# speedup vs baseline: 1.0329x; 1.0274x over previous
.Lmy_noperm_in:
	v_mfma_f32_16x16x32_f16 v[210:213], v[70:73], v[150:153], v[98:101]
	v_mfma_f32_16x16x32_f16 v[214:217], v[74:77], v[150:153], v[102:105]
	v_mfma_f32_16x16x32_f16 v[210:213], v[66:69], v[154:157], v[210:213]
	v_mfma_f32_16x16x32_f16 v[214:217], v[78:81], v[154:157], v[214:217]
	s_add_u32 s48, s20, 0x600000
	s_addc_u32 s49, s21, 0
	s_sub_u32 s50, s22, 0x600000
	s_mov_b32 s51, s23
	s_add_u32 s68, s16, 0xc000
	s_addc_u32 s69, s17, 0
	s_sub_u32 s70, s18, 0xc000
	s_mov_b32 s71, s19
	s_add_u32 s52, s20, 0x700000
	s_addc_u32 s53, s21, 0
	s_sub_u32 s54, s22, 0x700000
	s_mov_b32 s55, s23
	s_add_u32 s72, s16, 0x10000
	s_addc_u32 s73, s17, 0
	s_sub_u32 s74, s18, 0x10000
	s_mov_b32 s75, s19
	s_add_u32 s56, s20, 0x800000
	s_addc_u32 s57, s21, 0
	s_sub_u32 s58, s22, 0x800000
	s_mov_b32 s59, s23
	s_add_u32 s76, s16, 0x14000
	s_addc_u32 s77, s17, 0
	s_sub_u32 s78, s18, 0x14000
	s_mov_b32 s79, s19
	s_add_u32 s60, s20, 0x900000
	s_addc_u32 s61, s21, 0
	s_sub_u32 s62, s22, 0x900000
	s_mov_b32 s63, s23
	s_add_u32 s80, s16, 0x18000
	s_addc_u32 s81, s17, 0
	s_sub_u32 s82, s18, 0x18000
	s_mov_b32 s83, s19
	v_mfma_f32_16x16x32_f16 v[218:221], v[82:85], v[150:153], v[106:109]
	v_mfma_f32_16x16x32_f16 v[222:225], v[90:93], v[150:153], v[110:113]
	v_mfma_f32_16x16x32_f16 v[218:221], v[86:89], v[154:157], v[218:221]
	v_mfma_f32_16x16x32_f16 v[222:225], v[94:97], v[154:157], v[222:225]
	s_waitcnt lgkmcnt(2)
	s_waitcnt lgkmcnt(0)
	s_waitcnt vmcnt(9)
	v_cvt_pk_f16_f32 v251, v196, v197
	ds_write_b32 v1, v251 offset:4096
	ds_read_b128 v[150:153], v186 offset:2048
	ds_read_b128 v[154:157], v186 offset:3072
	s_add_i32 s45, s45, 0x100000
	s_add_i32 s46, s46, 0x4000
	s_movk_i32 s47, 0x0
	s_add_i32 s43, s40, -12
	s_lshl_b32 s43, s43, 12
	s_cmp_lt_u32 s40, 14
	s_cselect_b32 s43, s47, s43
	v_exp_f32_e32 v226, v210
	v_exp_f32_e32 v227, v211
	v_min_f32_e32 v228, s42, v212
	v_exp_f32_e32 v229, v213
	v_exp_f32_e32 v228, v228
	v_add_f32_e32 v227, 1.0, v227
	v_fma_f32 v230, v228, s41, s41
	v_rcp_f32_e32 v227, v227
	v_fma_f32 v230, v226, v230, v230
	v_rcp_f32_e32 v230, v230
	s_nop 0
	v_fma_f32 v226, -v228, v230, v230
	v_fma_f32 v200, v200, v227, v226
	v_exp_f32_e32 v226, v200
	s_nop 0
	v_add_f32_e32 v227, 1.0, v226
	v_fma_f32 v227, v229, v227, v227
	v_rcp_f32_e32 v227, v227
	s_nop 0
	v_fma_f32 v226, -v226, v227, v227
	v_exp_f32_e32 v231, v214
	v_exp_f32_e32 v232, v215
	v_min_f32_e32 v233, s42, v216
	v_exp_f32_e32 v234, v217
	v_exp_f32_e32 v233, v233
	v_exp_f32_e32 v236, v218
	v_add_f32_e32 v232, 1.0, v232
	v_fma_f32 v235, v233, s41, s41
	v_exp_f32_e32 v227, v219
	v_rcp_f32_e32 v232, v232
	v_fma_f32 v235, v231, v235, v235
	v_min_f32_e32 v228, s42, v220
	v_rcp_f32_e32 v235, v235
	s_nop 0
	v_fma_f32 v231, -v233, v235, v235
	v_exp_f32_e32 v229, v221
	v_fma_f32 v201, v201, v232, v231
	v_exp_f32_e32 v231, v201
	v_exp_f32_e32 v228, v228
	v_add_f32_e32 v232, 1.0, v231
	v_fma_f32 v232, v234, v232, v232
	v_add_f32_e32 v227, 1.0, v227
	v_rcp_f32_e32 v232, v232
	s_nop 0
	v_fma_f32 v231, -v231, v232, v232
	v_fma_f32 v230, v228, s41, s41
	v_cvt_pk_f16_f32 v246, v226, v231
	v_exp_f32_e32 v231, v222
	v_rcp_f32_e32 v227, v227
	v_exp_f32_e32 v232, v223
	buffer_load_dwordx4 v[138:141], v189, s[16:19], s46 offen
	buffer_load_dwordx4 v[142:145], v208, s[16:19], s46 offen
	v_min_f32_e32 v233, s42, v224
	v_fma_f32 v230, v236, v230, v230
	v_exp_f32_e32 v234, v225
	s_waitcnt lgkmcnt(0)
	v_mfma_f32_16x16x32_f16 v[210:213], v[70:73], v[150:153], v[98:101]
	v_exp_f32_e32 v233, v233
	v_rcp_f32_e32 v230, v230
	v_add_f32_e32 v232, 1.0, v232
	v_mfma_f32_16x16x32_f16 v[214:217], v[74:77], v[150:153], v[102:105]
	v_fma_f32 v235, v233, s41, s41
	v_fma_f32 v236, -v228, v230, v230
	v_rcp_f32_e32 v232, v232
	v_fma_f32 v235, v231, v235, v235
	v_fma_f32 v198, v198, v227, v236
	v_rcp_f32_e32 v235, v235
	s_nop 0
	v_fma_f32 v231, -v233, v235, v235
	v_exp_f32_e32 v236, v198
	v_fma_f32 v199, v199, v232, v231
	v_exp_f32_e32 v231, v199
	v_add_f32_e32 v227, 1.0, v236
	v_add_f32_e32 v232, 1.0, v231
	v_fma_f32 v232, v234, v232, v232
	v_fma_f32 v227, v229, v227, v227
	v_rcp_f32_e32 v232, v232
	s_nop 0
	v_fma_f32 v231, -v231, v232, v232
	v_rcp_f32_e32 v227, v227
	s_nop 0
	v_fma_f32 v236, -v236, v227, v227
	v_cvt_pk_f16_f32 v247, v236, v231
	ds_write_b64 v206, v[246:247] offset:8192
	v_mfma_f32_16x16x32_f16 v[210:213], v[66:69], v[154:157], v[210:213]
	v_mfma_f32_16x16x32_f16 v[214:217], v[78:81], v[154:157], v[214:217]
	v_mov_b32_e32 v174, v246
	v_mov_b32_e32 v175, v247
	buffer_load_dwordx2 v[196:197], v209, s[20:23], s45 offen
	s_add_i32 s40, s40, 1
	s_add_i32 s44, s44, 0x1000
	s_waitcnt lgkmcnt(0)
	s_barrier
	ds_read_b128 v[158:161], v252 offset:0
	ds_read_b128 v[162:165], v252 offset:1024
	ds_read_b128 v[166:169], v253 offset:2048
	ds_read_b128 v[170:173], v253 offset:3072
	v_mfma_f32_16x16x32_f16 v[218:221], v[82:85], v[150:153], v[106:109]
	v_mfma_f32_16x16x32_f16 v[222:225], v[90:93], v[150:153], v[110:113]
	v_mfma_f32_16x16x32_f16 v[218:221], v[86:89], v[154:157], v[218:221]
	v_mfma_f32_16x16x32_f16 v[222:225], v[94:97], v[154:157], v[222:225]
	s_waitcnt lgkmcnt(2)
	v_mfma_f32_16x16x32_f16 v[210:213], v[54:57], v[158:161], v[210:213]
	v_mfma_f32_16x16x32_f16 v[210:213], v[58:61], v[162:165], v[210:213]
	s_waitcnt lgkmcnt(0)
	v_mfma_f32_16x16x32_f16 v[210:213], v[62:65], v[166:169], v[210:213]
	v_mfma_f32_16x16x32_f16 v[210:213], v[50:53], v[170:173], v[210:213]
	s_waitcnt vmcnt(9)
	v_cvt_pk_f16_f32 v251, v194, v195
	ds_write_b32 v1, v251 offset:6144
	ds_read_b128 v[150:153], v186 offset:4096
	ds_read_b128 v[154:157], v186 offset:5120
	s_add_i32 s45, s45, 0x100000
	s_add_i32 s46, s46, 0x4000
	s_movk_i32 s47, 0x1000
	s_add_i32 s43, s40, -12
	s_lshl_b32 s43, s43, 12
	s_cmp_lt_u32 s40, 14
	s_cselect_b32 s43, s47, s43
	v_exp_f32_e32 v226, v210
	v_exp_f32_e32 v227, v211
	v_mfma_f32_16x16x32_f16 v[214:217], v[34:37], v[158:161], v[214:217]
	v_min_f32_e32 v228, s42, v212
	v_exp_f32_e32 v229, v213
	v_mfma_f32_16x16x32_f16 v[214:217], v[38:41], v[162:165], v[214:217]
	v_exp_f32_e32 v228, v228
	v_add_f32_e32 v227, 1.0, v227
	v_mfma_f32_16x16x32_f16 v[214:217], v[42:45], v[166:169], v[214:217]
	v_fma_f32 v230, v228, s41, s41
	v_rcp_f32_e32 v227, v227
	v_mfma_f32_16x16x32_f16 v[214:217], v[46:49], v[170:173], v[214:217]
	v_fma_f32 v230, v226, v230, v230
	v_rcp_f32_e32 v230, v230
	v_mfma_f32_16x16x32_f16 v[218:221], v[18:21], v[158:161], v[218:221]
	v_fma_f32 v226, -v228, v230, v230
	v_fma_f32 v200, v200, v227, v226
	v_mfma_f32_16x16x32_f16 v[218:221], v[14:17], v[162:165], v[218:221]
	v_exp_f32_e32 v226, v200
	s_nop 0
	v_add_f32_e32 v227, 1.0, v226
	v_mfma_f32_16x16x32_f16 v[218:221], v[10:13], v[166:169], v[218:221]
	v_fma_f32 v227, v229, v227, v227
	v_rcp_f32_e32 v227, v227
	v_mfma_f32_16x16x32_f16 v[218:221], v[26:29], v[170:173], v[218:221]
	v_fma_f32 v226, -v226, v227, v227
	v_exp_f32_e32 v231, v214
	v_mfma_f32_16x16x32_f16 v[222:225], v[2:5], v[158:161], v[222:225]
	v_exp_f32_e32 v232, v215
	v_min_f32_e32 v233, s42, v216
	v_mfma_f32_16x16x32_f16 v[222:225], v[6:9], v[162:165], v[222:225]
	v_exp_f32_e32 v234, v217
	v_exp_f32_e32 v233, v233
	v_mfma_f32_16x16x32_f16 v[222:225], v[22:25], v[166:169], v[222:225]
	v_exp_f32_e32 v236, v218
	v_add_f32_e32 v232, 1.0, v232
	v_mfma_f32_16x16x32_f16 v[222:225], v[30:33], v[170:173], v[222:225]
	v_fma_f32 v235, v233, s41, s41
	v_exp_f32_e32 v227, v219
	v_rcp_f32_e32 v232, v232
	v_fma_f32 v235, v231, v235, v235
	v_min_f32_e32 v228, s42, v220
	v_rcp_f32_e32 v235, v235
	s_nop 0
	v_fma_f32 v231, -v233, v235, v235
	v_exp_f32_e32 v229, v221
	v_fma_f32 v201, v201, v232, v231
	v_exp_f32_e32 v231, v201
	v_exp_f32_e32 v228, v228
	v_add_f32_e32 v232, 1.0, v231
	v_fma_f32 v232, v234, v232, v232
	v_add_f32_e32 v227, 1.0, v227
	v_rcp_f32_e32 v232, v232
	v_mfma_f32_16x16x32_f16 v[146:149], v[130:133], v[158:161], v[146:149]
	v_fma_f32 v231, -v231, v232, v232
	v_fma_f32 v230, v228, s41, s41
	v_cvt_pk_f16_f32 v246, v226, v231
	v_mfma_f32_16x16x32_f16 v[146:149], v[134:137], v[162:165], v[146:149]
	v_exp_f32_e32 v231, v222
	v_rcp_f32_e32 v227, v227
	v_exp_f32_e32 v232, v223
	buffer_load_dwordx4 v[130:133], v189, s[16:19], s46 offen
	buffer_load_dwordx4 v[134:137], v208, s[16:19], s46 offen
	v_min_f32_e32 v233, s42, v224
	v_fma_f32 v230, v236, v230, v230
	v_exp_f32_e32 v234, v225
	s_waitcnt lgkmcnt(0)
	v_mfma_f32_16x16x32_f16 v[210:213], v[70:73], v[150:153], v[98:101]
	v_exp_f32_e32 v233, v233
	v_rcp_f32_e32 v230, v230
	v_add_f32_e32 v232, 1.0, v232
	v_mfma_f32_16x16x32_f16 v[214:217], v[74:77], v[150:153], v[102:105]
	v_fma_f32 v235, v233, s41, s41
	v_fma_f32 v236, -v228, v230, v230
	v_rcp_f32_e32 v232, v232
	v_fma_f32 v235, v231, v235, v235
	v_fma_f32 v198, v198, v227, v236
	v_rcp_f32_e32 v235, v235
	s_nop 0
	v_fma_f32 v231, -v233, v235, v235
	v_exp_f32_e32 v236, v198
	v_fma_f32 v199, v199, v232, v231
	v_exp_f32_e32 v231, v199
	v_add_f32_e32 v227, 1.0, v236
	v_add_f32_e32 v232, 1.0, v231
	v_fma_f32 v232, v234, v232, v232
	v_fma_f32 v227, v229, v227, v227
	v_rcp_f32_e32 v232, v232
	s_nop 0
	v_fma_f32 v231, -v231, v232, v232
	v_rcp_f32_e32 v227, v227
	s_nop 0
	v_fma_f32 v236, -v236, v227, v227
	v_cvt_pk_f16_f32 v247, v236, v231
	ds_write_b64 v206, v[246:247] offset:12288
	v_mfma_f32_16x16x32_f16 v[210:213], v[66:69], v[154:157], v[210:213]
	v_mfma_f32_16x16x32_f16 v[214:217], v[78:81], v[154:157], v[214:217]
	v_mov_b32_e32 v176, v246
	v_mov_b32_e32 v177, v247
	buffer_load_dwordx2 v[194:195], v209, s[20:23], s45 offen
	s_add_i32 s40, s40, 1
	s_add_i32 s44, s44, 0x1000
	s_waitcnt lgkmcnt(0)
	s_barrier
	ds_read_b128 v[158:161], v252 offset:4096
	ds_read_b128 v[162:165], v252 offset:5120
	ds_read_b128 v[166:169], v253 offset:6144
	ds_read_b128 v[170:173], v253 offset:7168
	v_mfma_f32_16x16x32_f16 v[218:221], v[82:85], v[150:153], v[106:109]
	v_mfma_f32_16x16x32_f16 v[222:225], v[90:93], v[150:153], v[110:113]
	v_mfma_f32_16x16x32_f16 v[218:221], v[86:89], v[154:157], v[218:221]
	v_mfma_f32_16x16x32_f16 v[222:225], v[94:97], v[154:157], v[222:225]
	s_waitcnt lgkmcnt(2)
	v_mfma_f32_16x16x32_f16 v[210:213], v[54:57], v[158:161], v[210:213]
	v_mfma_f32_16x16x32_f16 v[210:213], v[58:61], v[162:165], v[210:213]
	s_waitcnt lgkmcnt(0)
	v_mfma_f32_16x16x32_f16 v[210:213], v[62:65], v[166:169], v[210:213]
	v_mfma_f32_16x16x32_f16 v[210:213], v[50:53], v[170:173], v[210:213]
	s_waitcnt vmcnt(9)
	v_cvt_pk_f16_f32 v251, v192, v193
	ds_write_b32 v1, v251 offset:0
	ds_read_b128 v[150:153], v186 offset:6144
	ds_read_b128 v[154:157], v186 offset:7168
	s_add_i32 s45, s45, 0x100000
	s_add_i32 s46, s46, 0x4000
	s_movk_i32 s47, 0x0
	s_add_i32 s43, s40, -12
	s_lshl_b32 s43, s43, 12
	s_cmp_lt_u32 s40, 14
	s_cselect_b32 s43, s47, s43
	v_exp_f32_e32 v226, v210
	v_exp_f32_e32 v227, v211
	v_mfma_f32_16x16x32_f16 v[214:217], v[34:37], v[158:161], v[214:217]
	v_min_f32_e32 v228, s42, v212
	v_exp_f32_e32 v229, v213
	v_mfma_f32_16x16x32_f16 v[214:217], v[38:41], v[162:165], v[214:217]
	v_exp_f32_e32 v228, v228
	v_add_f32_e32 v227, 1.0, v227
	v_mfma_f32_16x16x32_f16 v[214:217], v[42:45], v[166:169], v[214:217]
	v_fma_f32 v230, v228, s41, s41
	v_rcp_f32_e32 v227, v227
	v_mfma_f32_16x16x32_f16 v[214:217], v[46:49], v[170:173], v[214:217]
	v_fma_f32 v230, v226, v230, v230
	v_rcp_f32_e32 v230, v230
	v_mfma_f32_16x16x32_f16 v[218:221], v[18:21], v[158:161], v[218:221]
	v_fma_f32 v226, -v228, v230, v230
	v_fma_f32 v200, v200, v227, v226
	v_mfma_f32_16x16x32_f16 v[218:221], v[14:17], v[162:165], v[218:221]
	v_exp_f32_e32 v226, v200
	s_nop 0
	v_add_f32_e32 v227, 1.0, v226
	v_mfma_f32_16x16x32_f16 v[218:221], v[10:13], v[166:169], v[218:221]
	v_fma_f32 v227, v229, v227, v227
	v_rcp_f32_e32 v227, v227
	v_mfma_f32_16x16x32_f16 v[218:221], v[26:29], v[170:173], v[218:221]
	v_fma_f32 v226, -v226, v227, v227
	v_exp_f32_e32 v231, v214
	v_mfma_f32_16x16x32_f16 v[222:225], v[2:5], v[158:161], v[222:225]
	v_exp_f32_e32 v232, v215
	v_min_f32_e32 v233, s42, v216
	v_mfma_f32_16x16x32_f16 v[222:225], v[6:9], v[162:165], v[222:225]
	v_exp_f32_e32 v234, v217
	v_exp_f32_e32 v233, v233
	v_mfma_f32_16x16x32_f16 v[222:225], v[22:25], v[166:169], v[222:225]
	v_exp_f32_e32 v236, v218
	v_add_f32_e32 v232, 1.0, v232
	v_mfma_f32_16x16x32_f16 v[222:225], v[30:33], v[170:173], v[222:225]
	v_fma_f32 v235, v233, s41, s41
	v_exp_f32_e32 v227, v219
	v_rcp_f32_e32 v232, v232
	v_fma_f32 v235, v231, v235, v235
	v_min_f32_e32 v228, s42, v220
	v_rcp_f32_e32 v235, v235
	s_nop 0
	v_fma_f32 v231, -v233, v235, v235
	v_exp_f32_e32 v229, v221
	v_fma_f32 v201, v201, v232, v231
	v_exp_f32_e32 v231, v201
	v_exp_f32_e32 v228, v228
	v_add_f32_e32 v232, 1.0, v231
	v_fma_f32 v232, v234, v232, v232
	v_add_f32_e32 v227, 1.0, v227
	v_rcp_f32_e32 v232, v232
	v_mfma_f32_16x16x32_f16 v[146:149], v[122:125], v[158:161], v[146:149]
	v_fma_f32 v231, -v231, v232, v232
	v_fma_f32 v230, v228, s41, s41
	v_cvt_pk_f16_f32 v246, v226, v231
	v_mfma_f32_16x16x32_f16 v[146:149], v[126:129], v[162:165], v[146:149]
	v_exp_f32_e32 v231, v222
	v_rcp_f32_e32 v227, v227
	v_exp_f32_e32 v232, v223
	buffer_load_dwordx4 v[122:125], v189, s[16:19], s46 offen
	buffer_load_dwordx4 v[126:129], v208, s[16:19], s46 offen
	v_min_f32_e32 v233, s42, v224
	v_fma_f32 v230, v236, v230, v230
	v_exp_f32_e32 v234, v225
	s_waitcnt lgkmcnt(0)
	v_mfma_f32_16x16x32_f16 v[210:213], v[70:73], v[150:153], v[98:101]
	v_exp_f32_e32 v233, v233
	v_rcp_f32_e32 v230, v230
	v_add_f32_e32 v232, 1.0, v232
	v_mfma_f32_16x16x32_f16 v[214:217], v[74:77], v[150:153], v[102:105]
	v_fma_f32 v235, v233, s41, s41
	v_fma_f32 v236, -v228, v230, v230
	v_rcp_f32_e32 v232, v232
	v_fma_f32 v235, v231, v235, v235
	v_fma_f32 v198, v198, v227, v236
	v_rcp_f32_e32 v235, v235
	s_nop 0
	v_fma_f32 v231, -v233, v235, v235
	v_exp_f32_e32 v236, v198
	v_fma_f32 v199, v199, v232, v231
	v_exp_f32_e32 v231, v199
	v_add_f32_e32 v227, 1.0, v236
	v_add_f32_e32 v232, 1.0, v231
	v_fma_f32 v232, v234, v232, v232
	v_fma_f32 v227, v229, v227, v227
	v_rcp_f32_e32 v232, v232
	s_nop 0
	v_fma_f32 v231, -v231, v232, v232
	v_rcp_f32_e32 v227, v227
	s_nop 0
	v_fma_f32 v236, -v236, v227, v227
	v_cvt_pk_f16_f32 v247, v236, v231
	ds_write_b64 v206, v[246:247] offset:8192
	v_mfma_f32_16x16x32_f16 v[210:213], v[66:69], v[154:157], v[210:213]
	v_mfma_f32_16x16x32_f16 v[214:217], v[78:81], v[154:157], v[214:217]
	v_mov_b32_e32 v178, v246
	v_mov_b32_e32 v179, v247
	buffer_load_dwordx2 v[192:193], v209, s[20:23], s45 offen
	s_add_i32 s40, s40, 1
	s_add_i32 s44, s44, 0x1000
	s_waitcnt lgkmcnt(0)
	s_barrier
	ds_read_b128 v[158:161], v252 offset:0
	ds_read_b128 v[162:165], v252 offset:1024
	ds_read_b128 v[166:169], v253 offset:2048
	ds_read_b128 v[170:173], v253 offset:3072
	v_mfma_f32_16x16x32_f16 v[218:221], v[82:85], v[150:153], v[106:109]
	v_mfma_f32_16x16x32_f16 v[222:225], v[90:93], v[150:153], v[110:113]
	v_mfma_f32_16x16x32_f16 v[218:221], v[86:89], v[154:157], v[218:221]
	v_mfma_f32_16x16x32_f16 v[222:225], v[94:97], v[154:157], v[222:225]
	s_waitcnt lgkmcnt(2)
	v_mfma_f32_16x16x32_f16 v[210:213], v[54:57], v[158:161], v[210:213]
	v_mfma_f32_16x16x32_f16 v[210:213], v[58:61], v[162:165], v[210:213]
	s_waitcnt lgkmcnt(0)
	v_mfma_f32_16x16x32_f16 v[210:213], v[62:65], v[166:169], v[210:213]
	v_mfma_f32_16x16x32_f16 v[210:213], v[50:53], v[170:173], v[210:213]
	s_waitcnt vmcnt(9)
	v_cvt_pk_f16_f32 v251, v190, v191
	ds_write_b32 v1, v251 offset:2048
	ds_read_b128 v[150:153], v186 offset:0
	ds_read_b128 v[154:157], v186 offset:1024
	s_add_i32 s45, s45, 0x100000
	s_add_i32 s46, s46, 0x4000
	s_movk_i32 s47, 0x1000
	s_add_i32 s43, s40, -12
	s_lshl_b32 s43, s43, 12
	s_cmp_lt_u32 s40, 14
	s_cselect_b32 s43, s47, s43
	v_exp_f32_e32 v226, v210
	v_exp_f32_e32 v227, v211
	v_mfma_f32_16x16x32_f16 v[214:217], v[34:37], v[158:161], v[214:217]
	v_min_f32_e32 v228, s42, v212
	v_exp_f32_e32 v229, v213
	v_mfma_f32_16x16x32_f16 v[214:217], v[38:41], v[162:165], v[214:217]
	v_exp_f32_e32 v228, v228
	v_add_f32_e32 v227, 1.0, v227
	v_mfma_f32_16x16x32_f16 v[214:217], v[42:45], v[166:169], v[214:217]
	v_fma_f32 v230, v228, s41, s41
	v_rcp_f32_e32 v227, v227
	v_mfma_f32_16x16x32_f16 v[214:217], v[46:49], v[170:173], v[214:217]
	v_fma_f32 v230, v226, v230, v230
	v_rcp_f32_e32 v230, v230
	v_mfma_f32_16x16x32_f16 v[218:221], v[18:21], v[158:161], v[218:221]
	v_fma_f32 v226, -v228, v230, v230
	v_fma_f32 v200, v200, v227, v226
	v_mfma_f32_16x16x32_f16 v[218:221], v[14:17], v[162:165], v[218:221]
	v_exp_f32_e32 v226, v200
	s_nop 0
	v_add_f32_e32 v227, 1.0, v226
	v_mfma_f32_16x16x32_f16 v[218:221], v[10:13], v[166:169], v[218:221]
	v_fma_f32 v227, v229, v227, v227
	v_rcp_f32_e32 v227, v227
	v_mfma_f32_16x16x32_f16 v[218:221], v[26:29], v[170:173], v[218:221]
	v_fma_f32 v226, -v226, v227, v227
	v_exp_f32_e32 v231, v214
	v_mfma_f32_16x16x32_f16 v[222:225], v[2:5], v[158:161], v[222:225]
	v_exp_f32_e32 v232, v215
	v_min_f32_e32 v233, s42, v216
	v_mfma_f32_16x16x32_f16 v[222:225], v[6:9], v[162:165], v[222:225]
	v_exp_f32_e32 v234, v217
	v_exp_f32_e32 v233, v233
	v_mfma_f32_16x16x32_f16 v[222:225], v[22:25], v[166:169], v[222:225]
	v_exp_f32_e32 v236, v218
	v_add_f32_e32 v232, 1.0, v232
	v_mfma_f32_16x16x32_f16 v[222:225], v[30:33], v[170:173], v[222:225]
	v_fma_f32 v235, v233, s41, s41
	v_exp_f32_e32 v227, v219
	v_rcp_f32_e32 v232, v232
	v_fma_f32 v235, v231, v235, v235
	v_min_f32_e32 v228, s42, v220
	v_rcp_f32_e32 v235, v235
	s_nop 0
	v_fma_f32 v231, -v233, v235, v235
	v_exp_f32_e32 v229, v221
	v_fma_f32 v201, v201, v232, v231
	v_exp_f32_e32 v231, v201
	v_exp_f32_e32 v228, v228
	v_add_f32_e32 v232, 1.0, v231
	v_fma_f32 v232, v234, v232, v232
	v_add_f32_e32 v227, 1.0, v227
	v_rcp_f32_e32 v232, v232
	v_mfma_f32_16x16x32_f16 v[146:149], v[114:117], v[158:161], v[146:149]
	v_fma_f32 v231, -v231, v232, v232
	v_fma_f32 v230, v228, s41, s41
	v_cvt_pk_f16_f32 v246, v226, v231
	v_mfma_f32_16x16x32_f16 v[146:149], v[118:121], v[162:165], v[146:149]
	v_exp_f32_e32 v231, v222
	v_rcp_f32_e32 v227, v227
	v_exp_f32_e32 v232, v223
	buffer_load_dwordx4 v[114:117], v189, s[16:19], s46 offen
	buffer_load_dwordx4 v[118:121], v208, s[16:19], s46 offen
	v_min_f32_e32 v233, s42, v224
	v_fma_f32 v230, v236, v230, v230
	v_exp_f32_e32 v234, v225
	s_waitcnt lgkmcnt(0)
	v_mfma_f32_16x16x32_f16 v[210:213], v[70:73], v[150:153], v[98:101]
	v_exp_f32_e32 v233, v233
	v_rcp_f32_e32 v230, v230
	v_add_f32_e32 v232, 1.0, v232
	v_mfma_f32_16x16x32_f16 v[214:217], v[74:77], v[150:153], v[102:105]
	v_fma_f32 v235, v233, s41, s41
	v_fma_f32 v236, -v228, v230, v230
	v_rcp_f32_e32 v232, v232
	v_fma_f32 v235, v231, v235, v235
	v_fma_f32 v198, v198, v227, v236
	v_rcp_f32_e32 v235, v235
	s_nop 0
	v_fma_f32 v231, -v233, v235, v235
	v_exp_f32_e32 v236, v198
	v_fma_f32 v199, v199, v232, v231
	v_exp_f32_e32 v231, v199
	v_add_f32_e32 v227, 1.0, v236
	v_add_f32_e32 v232, 1.0, v231
	v_fma_f32 v232, v234, v232, v232
	v_fma_f32 v227, v229, v227, v227
	v_rcp_f32_e32 v232, v232
	s_nop 0
	v_fma_f32 v231, -v231, v232, v232
	v_rcp_f32_e32 v227, v227
	s_nop 0
	v_fma_f32 v236, -v236, v227, v227
	v_cvt_pk_f16_f32 v247, v236, v231
	ds_write_b64 v206, v[246:247] offset:12288
	v_mfma_f32_16x16x32_f16 v[210:213], v[66:69], v[154:157], v[210:213]
	v_mfma_f32_16x16x32_f16 v[214:217], v[78:81], v[154:157], v[214:217]
	v_mov_b32_e32 v180, v246
	v_mov_b32_e32 v181, v247
	buffer_load_dwordx2 v[190:191], v209, s[20:23], s45 offen
	s_add_i32 s40, s40, 1
	s_add_i32 s44, s44, 0x1000
	s_waitcnt lgkmcnt(0)
	s_barrier
	ds_read_b128 v[158:161], v252 offset:4096
	ds_read_b128 v[162:165], v252 offset:5120
	ds_read_b128 v[166:169], v253 offset:6144
	ds_read_b128 v[170:173], v253 offset:7168
	v_mfma_f32_16x16x32_f16 v[218:221], v[82:85], v[150:153], v[106:109]
	v_mfma_f32_16x16x32_f16 v[222:225], v[90:93], v[150:153], v[110:113]
	v_mfma_f32_16x16x32_f16 v[218:221], v[86:89], v[154:157], v[218:221]
	v_mfma_f32_16x16x32_f16 v[222:225], v[94:97], v[154:157], v[222:225]
	s_waitcnt lgkmcnt(2)
	v_mfma_f32_16x16x32_f16 v[210:213], v[54:57], v[158:161], v[210:213]
	v_mfma_f32_16x16x32_f16 v[210:213], v[58:61], v[162:165], v[210:213]
	s_waitcnt lgkmcnt(0)
	v_mfma_f32_16x16x32_f16 v[210:213], v[62:65], v[166:169], v[210:213]
	v_mfma_f32_16x16x32_f16 v[210:213], v[50:53], v[170:173], v[210:213]
	s_waitcnt vmcnt(9)
	v_cvt_pk_f16_f32 v251, v196, v197
	ds_write_b32 v1, v251 offset:4096
	ds_read_b128 v[150:153], v186 offset:2048
	ds_read_b128 v[154:157], v186 offset:3072
	s_add_i32 s45, s45, 0x100000
	s_add_i32 s46, s46, 0x4000
	s_movk_i32 s47, 0x0
	s_add_i32 s43, s40, -12
	s_lshl_b32 s43, s43, 12
	s_cmp_lt_u32 s40, 14
	s_cselect_b32 s43, s47, s43
	v_exp_f32_e32 v226, v210
	v_exp_f32_e32 v227, v211
	v_mfma_f32_16x16x32_f16 v[214:217], v[34:37], v[158:161], v[214:217]
	v_min_f32_e32 v228, s42, v212
	v_exp_f32_e32 v229, v213
	v_mfma_f32_16x16x32_f16 v[214:217], v[38:41], v[162:165], v[214:217]
	v_exp_f32_e32 v228, v228
	v_add_f32_e32 v227, 1.0, v227
	v_mfma_f32_16x16x32_f16 v[214:217], v[42:45], v[166:169], v[214:217]
	v_fma_f32 v230, v228, s41, s41
	v_rcp_f32_e32 v227, v227
	v_mfma_f32_16x16x32_f16 v[214:217], v[46:49], v[170:173], v[214:217]
	v_fma_f32 v230, v226, v230, v230
	v_rcp_f32_e32 v230, v230
	v_mfma_f32_16x16x32_f16 v[218:221], v[18:21], v[158:161], v[218:221]
	v_fma_f32 v226, -v228, v230, v230
	v_fma_f32 v200, v200, v227, v226
	v_mfma_f32_16x16x32_f16 v[218:221], v[14:17], v[162:165], v[218:221]
	v_exp_f32_e32 v226, v200
	s_nop 0
	v_add_f32_e32 v227, 1.0, v226
	v_mfma_f32_16x16x32_f16 v[218:221], v[10:13], v[166:169], v[218:221]
	v_fma_f32 v227, v229, v227, v227
	v_rcp_f32_e32 v227, v227
	v_mfma_f32_16x16x32_f16 v[218:221], v[26:29], v[170:173], v[218:221]
	v_fma_f32 v226, -v226, v227, v227
	v_exp_f32_e32 v231, v214
	v_mfma_f32_16x16x32_f16 v[222:225], v[2:5], v[158:161], v[222:225]
	v_exp_f32_e32 v232, v215
	v_min_f32_e32 v233, s42, v216
	v_mfma_f32_16x16x32_f16 v[222:225], v[6:9], v[162:165], v[222:225]
	v_exp_f32_e32 v234, v217
	v_exp_f32_e32 v233, v233
	v_mfma_f32_16x16x32_f16 v[222:225], v[22:25], v[166:169], v[222:225]
	v_exp_f32_e32 v236, v218
	v_add_f32_e32 v232, 1.0, v232
	v_mfma_f32_16x16x32_f16 v[222:225], v[30:33], v[170:173], v[222:225]
	v_fma_f32 v235, v233, s41, s41
	v_exp_f32_e32 v227, v219
	v_rcp_f32_e32 v232, v232
	v_fma_f32 v235, v231, v235, v235
	v_min_f32_e32 v228, s42, v220
	v_rcp_f32_e32 v235, v235
	s_nop 0
	v_fma_f32 v231, -v233, v235, v235
	v_exp_f32_e32 v229, v221
	v_fma_f32 v201, v201, v232, v231
	v_exp_f32_e32 v231, v201
	v_exp_f32_e32 v228, v228
	v_add_f32_e32 v232, 1.0, v231
	v_fma_f32 v232, v234, v232, v232
	v_add_f32_e32 v227, 1.0, v227
	v_rcp_f32_e32 v232, v232
	v_mfma_f32_16x16x32_f16 v[146:149], v[138:141], v[158:161], v[146:149]
	v_fma_f32 v231, -v231, v232, v232
	v_fma_f32 v230, v228, s41, s41
	v_cvt_pk_f16_f32 v246, v226, v231
	v_mfma_f32_16x16x32_f16 v[146:149], v[142:145], v[162:165], v[146:149]
	v_exp_f32_e32 v231, v222
	v_rcp_f32_e32 v227, v227
	v_exp_f32_e32 v232, v223
	buffer_load_dwordx4 v[138:141], v189, s[16:19], s46 offen
	buffer_load_dwordx4 v[142:145], v208, s[16:19], s46 offen
	v_min_f32_e32 v233, s42, v224
	v_fma_f32 v230, v236, v230, v230
	v_exp_f32_e32 v234, v225
	s_waitcnt lgkmcnt(0)
	v_mfma_f32_16x16x32_f16 v[210:213], v[70:73], v[150:153], v[98:101]
	v_exp_f32_e32 v233, v233
	v_rcp_f32_e32 v230, v230
	v_add_f32_e32 v232, 1.0, v232
	v_mfma_f32_16x16x32_f16 v[214:217], v[74:77], v[150:153], v[102:105]
	v_fma_f32 v235, v233, s41, s41
	v_fma_f32 v236, -v228, v230, v230
	v_rcp_f32_e32 v232, v232
	v_fma_f32 v235, v231, v235, v235
	v_fma_f32 v198, v198, v227, v236
	v_rcp_f32_e32 v235, v235
	s_nop 0
	v_fma_f32 v231, -v233, v235, v235
	v_exp_f32_e32 v236, v198
	v_fma_f32 v199, v199, v232, v231
	v_exp_f32_e32 v231, v199
	v_add_f32_e32 v227, 1.0, v236
	v_add_f32_e32 v232, 1.0, v231
	v_fma_f32 v232, v234, v232, v232
	v_fma_f32 v227, v229, v227, v227
	v_rcp_f32_e32 v232, v232
	s_nop 0
	v_fma_f32 v231, -v231, v232, v232
	v_rcp_f32_e32 v227, v227
	s_nop 0
	v_fma_f32 v236, -v236, v227, v227
	v_cvt_pk_f16_f32 v247, v236, v231
	ds_write_b64 v206, v[246:247] offset:8192
	v_mfma_f32_16x16x32_f16 v[210:213], v[66:69], v[154:157], v[210:213]
	v_mfma_f32_16x16x32_f16 v[214:217], v[78:81], v[154:157], v[214:217]
	v_mov_b32_e32 v182, v246
	v_mov_b32_e32 v183, v247
	buffer_load_dwordx2 v[196:197], v209, s[20:23], s45 offen
	s_add_i32 s40, s40, 1
	s_add_i32 s44, s44, 0x1000
	s_waitcnt lgkmcnt(0)
	s_barrier
	ds_read_b128 v[158:161], v252 offset:0
	ds_read_b128 v[162:165], v252 offset:1024
	ds_read_b128 v[166:169], v253 offset:2048
	ds_read_b128 v[170:173], v253 offset:3072
	v_mfma_f32_16x16x32_f16 v[218:221], v[82:85], v[150:153], v[106:109]
	v_mfma_f32_16x16x32_f16 v[222:225], v[90:93], v[150:153], v[110:113]
	v_mfma_f32_16x16x32_f16 v[218:221], v[86:89], v[154:157], v[218:221]
	v_mfma_f32_16x16x32_f16 v[222:225], v[94:97], v[154:157], v[222:225]
	s_waitcnt lgkmcnt(2)
	v_mfma_f32_16x16x32_f16 v[210:213], v[54:57], v[158:161], v[210:213]
	v_mfma_f32_16x16x32_f16 v[210:213], v[58:61], v[162:165], v[210:213]
	s_waitcnt lgkmcnt(0)
	v_mfma_f32_16x16x32_f16 v[210:213], v[62:65], v[166:169], v[210:213]
	v_mfma_f32_16x16x32_f16 v[210:213], v[50:53], v[170:173], v[210:213]
	s_waitcnt vmcnt(9)
	v_cvt_pk_f16_f32 v251, v194, v195
	ds_write_b32 v1, v251 offset:6144
	ds_read_b128 v[150:153], v186 offset:4096
	ds_read_b128 v[154:157], v186 offset:5120
	s_add_i32 s45, s45, 0x100000
	s_add_i32 s46, s46, 0x4000
	s_movk_i32 s47, 0x1000
	s_add_i32 s43, s40, -12
	s_lshl_b32 s43, s43, 12
	s_cmp_lt_u32 s40, 14
	s_cselect_b32 s43, s47, s43
	v_exp_f32_e32 v226, v210
	v_exp_f32_e32 v227, v211
	v_mfma_f32_16x16x32_f16 v[214:217], v[34:37], v[158:161], v[214:217]
	v_min_f32_e32 v228, s42, v212
	v_exp_f32_e32 v229, v213
	v_mfma_f32_16x16x32_f16 v[214:217], v[38:41], v[162:165], v[214:217]
	v_exp_f32_e32 v228, v228
	v_add_f32_e32 v227, 1.0, v227
	v_mfma_f32_16x16x32_f16 v[214:217], v[42:45], v[166:169], v[214:217]
	v_fma_f32 v230, v228, s41, s41
	v_rcp_f32_e32 v227, v227
	v_mfma_f32_16x16x32_f16 v[214:217], v[46:49], v[170:173], v[214:217]
	v_fma_f32 v230, v226, v230, v230
	v_rcp_f32_e32 v230, v230
	v_mfma_f32_16x16x32_f16 v[218:221], v[18:21], v[158:161], v[218:221]
	v_fma_f32 v226, -v228, v230, v230
	v_fma_f32 v200, v200, v227, v226
	v_mfma_f32_16x16x32_f16 v[218:221], v[14:17], v[162:165], v[218:221]
	v_exp_f32_e32 v226, v200
	s_nop 0
	v_add_f32_e32 v227, 1.0, v226
	v_mfma_f32_16x16x32_f16 v[218:221], v[10:13], v[166:169], v[218:221]
	v_fma_f32 v227, v229, v227, v227
	v_rcp_f32_e32 v227, v227
	v_mfma_f32_16x16x32_f16 v[218:221], v[26:29], v[170:173], v[218:221]
	v_fma_f32 v226, -v226, v227, v227
	v_exp_f32_e32 v231, v214
	v_mfma_f32_16x16x32_f16 v[222:225], v[2:5], v[158:161], v[222:225]
	v_exp_f32_e32 v232, v215
	v_min_f32_e32 v233, s42, v216
	v_mfma_f32_16x16x32_f16 v[222:225], v[6:9], v[162:165], v[222:225]
	v_exp_f32_e32 v234, v217
	v_exp_f32_e32 v233, v233
	v_mfma_f32_16x16x32_f16 v[222:225], v[22:25], v[166:169], v[222:225]
	v_exp_f32_e32 v236, v218
	v_add_f32_e32 v232, 1.0, v232
	v_mfma_f32_16x16x32_f16 v[222:225], v[30:33], v[170:173], v[222:225]
	v_fma_f32 v235, v233, s41, s41
	v_exp_f32_e32 v227, v219
	v_rcp_f32_e32 v232, v232
	v_fma_f32 v235, v231, v235, v235
	v_min_f32_e32 v228, s42, v220
	v_rcp_f32_e32 v235, v235
	s_nop 0
	v_fma_f32 v231, -v233, v235, v235
	v_exp_f32_e32 v229, v221
	v_fma_f32 v201, v201, v232, v231
	v_exp_f32_e32 v231, v201
	v_exp_f32_e32 v228, v228
	v_add_f32_e32 v232, 1.0, v231
	v_fma_f32 v232, v234, v232, v232
	v_add_f32_e32 v227, 1.0, v227
	v_rcp_f32_e32 v232, v232
	v_mfma_f32_16x16x32_f16 v[146:149], v[130:133], v[158:161], v[146:149]
	v_fma_f32 v231, -v231, v232, v232
	v_fma_f32 v230, v228, s41, s41
	v_cvt_pk_f16_f32 v246, v226, v231
	v_mfma_f32_16x16x32_f16 v[146:149], v[134:137], v[162:165], v[146:149]
	v_exp_f32_e32 v231, v222
	v_rcp_f32_e32 v227, v227
	v_exp_f32_e32 v232, v223
	buffer_load_dwordx4 v[130:133], v189, s[16:19], s46 offen
	buffer_load_dwordx4 v[134:137], v208, s[16:19], s46 offen
	v_min_f32_e32 v233, s42, v224
	v_fma_f32 v230, v236, v230, v230
	v_exp_f32_e32 v234, v225
	s_waitcnt lgkmcnt(0)
	v_mfma_f32_16x16x32_f16 v[210:213], v[70:73], v[150:153], v[98:101]
	v_exp_f32_e32 v233, v233
	v_rcp_f32_e32 v230, v230
	v_add_f32_e32 v232, 1.0, v232
	v_mfma_f32_16x16x32_f16 v[214:217], v[74:77], v[150:153], v[102:105]
	v_fma_f32 v235, v233, s41, s41
	v_fma_f32 v236, -v228, v230, v230
	v_rcp_f32_e32 v232, v232
	v_fma_f32 v235, v231, v235, v235
	v_fma_f32 v198, v198, v227, v236
	v_rcp_f32_e32 v235, v235
	s_nop 0
	v_fma_f32 v231, -v233, v235, v235
	v_exp_f32_e32 v236, v198
	v_fma_f32 v199, v199, v232, v231
	v_exp_f32_e32 v231, v199
	v_add_f32_e32 v227, 1.0, v236
	v_add_f32_e32 v232, 1.0, v231
	v_fma_f32 v232, v234, v232, v232
	v_fma_f32 v227, v229, v227, v227
	v_rcp_f32_e32 v232, v232
	s_nop 0
	v_fma_f32 v231, -v231, v232, v232
	v_rcp_f32_e32 v227, v227
	s_nop 0
	v_fma_f32 v236, -v236, v227, v227
	v_cvt_pk_f16_f32 v247, v236, v231
	ds_write_b64 v206, v[246:247] offset:12288
	v_mfma_f32_16x16x32_f16 v[210:213], v[66:69], v[154:157], v[210:213]
	v_mfma_f32_16x16x32_f16 v[214:217], v[78:81], v[154:157], v[214:217]
	v_mov_b32_e32 v184, v246
	v_mov_b32_e32 v185, v247
	buffer_load_dwordx2 v[194:195], v209, s[20:23], s45 offen
	s_add_i32 s40, s40, 1
	s_add_i32 s44, s44, 0x1000
	s_waitcnt lgkmcnt(0)
	s_barrier
	ds_read_b128 v[158:161], v252 offset:4096
	ds_read_b128 v[162:165], v252 offset:5120
	ds_read_b128 v[166:169], v253 offset:6144
	ds_read_b128 v[170:173], v253 offset:7168
	v_mfma_f32_16x16x32_f16 v[218:221], v[82:85], v[150:153], v[106:109]
	v_mfma_f32_16x16x32_f16 v[222:225], v[90:93], v[150:153], v[110:113]
	v_mfma_f32_16x16x32_f16 v[218:221], v[86:89], v[154:157], v[218:221]
	v_mfma_f32_16x16x32_f16 v[222:225], v[94:97], v[154:157], v[222:225]
	s_waitcnt lgkmcnt(2)
	v_mfma_f32_16x16x32_f16 v[210:213], v[54:57], v[158:161], v[210:213]
	v_mfma_f32_16x16x32_f16 v[210:213], v[58:61], v[162:165], v[210:213]
	s_waitcnt lgkmcnt(0)
	v_mfma_f32_16x16x32_f16 v[210:213], v[62:65], v[166:169], v[210:213]
	v_mfma_f32_16x16x32_f16 v[210:213], v[50:53], v[170:173], v[210:213]
	s_waitcnt vmcnt(9)
	v_cvt_pk_f16_f32 v251, v192, v193
	ds_write_b32 v1, v251 offset:0
	ds_read_b128 v[150:153], v186 offset:6144
	ds_read_b128 v[154:157], v186 offset:7168
	s_add_i32 s45, s45, 0x100000
	s_add_i32 s46, s46, 0x4000
	s_movk_i32 s47, 0x0
	s_add_i32 s43, s40, -12
	s_lshl_b32 s43, s43, 12
	s_cmp_lt_u32 s40, 14
	s_cselect_b32 s43, s47, s43
	v_exp_f32_e32 v226, v210
	v_exp_f32_e32 v227, v211
	v_mfma_f32_16x16x32_f16 v[214:217], v[34:37], v[158:161], v[214:217]
	v_min_f32_e32 v228, s42, v212
	v_exp_f32_e32 v229, v213
	v_mfma_f32_16x16x32_f16 v[214:217], v[38:41], v[162:165], v[214:217]
	v_exp_f32_e32 v228, v228
	v_add_f32_e32 v227, 1.0, v227
	v_mfma_f32_16x16x32_f16 v[214:217], v[42:45], v[166:169], v[214:217]
	v_fma_f32 v230, v228, s41, s41
	v_rcp_f32_e32 v227, v227
	v_mfma_f32_16x16x32_f16 v[214:217], v[46:49], v[170:173], v[214:217]
	v_fma_f32 v230, v226, v230, v230
	v_rcp_f32_e32 v230, v230
	v_mfma_f32_16x16x32_f16 v[218:221], v[18:21], v[158:161], v[218:221]
	v_fma_f32 v226, -v228, v230, v230
	v_fma_f32 v200, v200, v227, v226
	v_mfma_f32_16x16x32_f16 v[218:221], v[14:17], v[162:165], v[218:221]
	v_exp_f32_e32 v226, v200
	s_nop 0
	v_add_f32_e32 v227, 1.0, v226
	v_mfma_f32_16x16x32_f16 v[218:221], v[10:13], v[166:169], v[218:221]
	v_fma_f32 v227, v229, v227, v227
	v_rcp_f32_e32 v227, v227
	v_mfma_f32_16x16x32_f16 v[218:221], v[26:29], v[170:173], v[218:221]
	v_fma_f32 v226, -v226, v227, v227
	v_exp_f32_e32 v231, v214
	v_mfma_f32_16x16x32_f16 v[222:225], v[2:5], v[158:161], v[222:225]
	v_exp_f32_e32 v232, v215
	v_min_f32_e32 v233, s42, v216
	v_mfma_f32_16x16x32_f16 v[222:225], v[6:9], v[162:165], v[222:225]
	v_exp_f32_e32 v234, v217
	v_exp_f32_e32 v233, v233
	v_mfma_f32_16x16x32_f16 v[222:225], v[22:25], v[166:169], v[222:225]
	v_exp_f32_e32 v236, v218
	v_add_f32_e32 v232, 1.0, v232
	v_mfma_f32_16x16x32_f16 v[222:225], v[30:33], v[170:173], v[222:225]
	v_fma_f32 v235, v233, s41, s41
	v_exp_f32_e32 v227, v219
	v_rcp_f32_e32 v232, v232
	v_fma_f32 v235, v231, v235, v235
	v_min_f32_e32 v228, s42, v220
	v_rcp_f32_e32 v235, v235
	s_nop 0
	v_fma_f32 v231, -v233, v235, v235
	v_exp_f32_e32 v229, v221
	v_fma_f32 v201, v201, v232, v231
	v_exp_f32_e32 v231, v201
	v_exp_f32_e32 v228, v228
	v_add_f32_e32 v232, 1.0, v231
	v_fma_f32 v232, v234, v232, v232
	v_add_f32_e32 v227, 1.0, v227
	v_rcp_f32_e32 v232, v232
	v_mfma_f32_16x16x32_f16 v[146:149], v[122:125], v[158:161], v[146:149]
	v_fma_f32 v231, -v231, v232, v232
	v_fma_f32 v230, v228, s41, s41
	v_cvt_pk_f16_f32 v246, v226, v231
	v_mfma_f32_16x16x32_f16 v[146:149], v[126:129], v[162:165], v[146:149]
	v_exp_f32_e32 v231, v222
	v_rcp_f32_e32 v227, v227
	v_exp_f32_e32 v232, v223
	buffer_load_dwordx4 v[122:125], v189, s[16:19], s46 offen
	buffer_load_dwordx4 v[126:129], v208, s[16:19], s46 offen
	v_min_f32_e32 v233, s42, v224
	v_fma_f32 v230, v236, v230, v230
	v_exp_f32_e32 v234, v225
	s_waitcnt lgkmcnt(0)
	v_mfma_f32_16x16x32_f16 v[210:213], v[70:73], v[150:153], v[98:101]
	v_exp_f32_e32 v233, v233
	v_rcp_f32_e32 v230, v230
	v_add_f32_e32 v232, 1.0, v232
	v_mfma_f32_16x16x32_f16 v[214:217], v[74:77], v[150:153], v[102:105]
	v_fma_f32 v235, v233, s41, s41
	v_fma_f32 v236, -v228, v230, v230
	v_rcp_f32_e32 v232, v232
	v_fma_f32 v235, v231, v235, v235
	v_fma_f32 v198, v198, v227, v236
	v_rcp_f32_e32 v235, v235
	s_nop 0
	v_fma_f32 v231, -v233, v235, v235
	v_exp_f32_e32 v236, v198
	v_fma_f32 v199, v199, v232, v231
	v_exp_f32_e32 v231, v199
	v_add_f32_e32 v227, 1.0, v236
	v_add_f32_e32 v232, 1.0, v231
	v_fma_f32 v232, v234, v232, v232
	v_fma_f32 v227, v229, v227, v227
	v_rcp_f32_e32 v232, v232
	s_nop 0
	v_fma_f32 v231, -v231, v232, v232
	v_rcp_f32_e32 v227, v227
	s_nop 0
	v_fma_f32 v236, -v236, v227, v227
	v_cvt_pk_f16_f32 v247, v236, v231
	ds_write_b64 v206, v[246:247] offset:8192
	v_mfma_f32_16x16x32_f16 v[210:213], v[66:69], v[154:157], v[210:213]
	v_mfma_f32_16x16x32_f16 v[214:217], v[78:81], v[154:157], v[214:217]
	v_mov_b32_e32 v237, v246
	v_mov_b32_e32 v238, v247
	buffer_load_dwordx2 v[192:193], v209, s[20:23], s45 offen
	s_add_i32 s40, s40, 1
	s_add_i32 s44, s44, 0x1000
	s_waitcnt lgkmcnt(0)
	s_barrier
	ds_read_b128 v[158:161], v252 offset:0
	ds_read_b128 v[162:165], v252 offset:1024
	ds_read_b128 v[166:169], v253 offset:2048
	ds_read_b128 v[170:173], v253 offset:3072
	v_mfma_f32_16x16x32_f16 v[218:221], v[82:85], v[150:153], v[106:109]
	v_mfma_f32_16x16x32_f16 v[222:225], v[90:93], v[150:153], v[110:113]
	v_mfma_f32_16x16x32_f16 v[218:221], v[86:89], v[154:157], v[218:221]
	v_mfma_f32_16x16x32_f16 v[222:225], v[94:97], v[154:157], v[222:225]
	s_waitcnt lgkmcnt(2)
	v_mfma_f32_16x16x32_f16 v[210:213], v[54:57], v[158:161], v[210:213]
	v_mfma_f32_16x16x32_f16 v[210:213], v[58:61], v[162:165], v[210:213]
	s_waitcnt lgkmcnt(0)
	v_mfma_f32_16x16x32_f16 v[210:213], v[62:65], v[166:169], v[210:213]
	v_mfma_f32_16x16x32_f16 v[210:213], v[50:53], v[170:173], v[210:213]
	s_waitcnt vmcnt(9)
	v_cvt_pk_f16_f32 v251, v190, v191
	ds_write_b32 v1, v251 offset:2048
	ds_read_b128 v[150:153], v186 offset:0
	ds_read_b128 v[154:157], v186 offset:1024
	s_add_i32 s45, s45, 0x100000
	s_add_i32 s46, s46, 0x4000
	s_movk_i32 s47, 0x1000
	s_add_i32 s43, s40, -12
	s_lshl_b32 s43, s43, 12
	s_cmp_lt_u32 s40, 14
	s_cselect_b32 s43, s47, s43
	v_exp_f32_e32 v226, v210
	v_exp_f32_e32 v227, v211
	v_mfma_f32_16x16x32_f16 v[214:217], v[34:37], v[158:161], v[214:217]
	v_min_f32_e32 v228, s42, v212
	v_exp_f32_e32 v229, v213
	v_mfma_f32_16x16x32_f16 v[214:217], v[38:41], v[162:165], v[214:217]
	v_exp_f32_e32 v228, v228
	v_add_f32_e32 v227, 1.0, v227
	v_mfma_f32_16x16x32_f16 v[214:217], v[42:45], v[166:169], v[214:217]
	v_fma_f32 v230, v228, s41, s41
	v_rcp_f32_e32 v227, v227
	v_mfma_f32_16x16x32_f16 v[214:217], v[46:49], v[170:173], v[214:217]
	v_fma_f32 v230, v226, v230, v230
	v_rcp_f32_e32 v230, v230
	v_mfma_f32_16x16x32_f16 v[218:221], v[18:21], v[158:161], v[218:221]
	v_fma_f32 v226, -v228, v230, v230
	v_fma_f32 v200, v200, v227, v226
	v_mfma_f32_16x16x32_f16 v[218:221], v[14:17], v[162:165], v[218:221]
	v_exp_f32_e32 v226, v200
	s_nop 0
	v_add_f32_e32 v227, 1.0, v226
	v_mfma_f32_16x16x32_f16 v[218:221], v[10:13], v[166:169], v[218:221]
	v_fma_f32 v227, v229, v227, v227
	v_rcp_f32_e32 v227, v227
	v_mfma_f32_16x16x32_f16 v[218:221], v[26:29], v[170:173], v[218:221]
	v_fma_f32 v226, -v226, v227, v227
	v_exp_f32_e32 v231, v214
	v_mfma_f32_16x16x32_f16 v[222:225], v[2:5], v[158:161], v[222:225]
	v_exp_f32_e32 v232, v215
	v_min_f32_e32 v233, s42, v216
	v_mfma_f32_16x16x32_f16 v[222:225], v[6:9], v[162:165], v[222:225]
	v_exp_f32_e32 v234, v217
	v_exp_f32_e32 v233, v233
	v_mfma_f32_16x16x32_f16 v[222:225], v[22:25], v[166:169], v[222:225]
	v_exp_f32_e32 v236, v218
	v_add_f32_e32 v232, 1.0, v232
	v_mfma_f32_16x16x32_f16 v[222:225], v[30:33], v[170:173], v[222:225]
	v_fma_f32 v235, v233, s41, s41
	v_exp_f32_e32 v227, v219
	v_rcp_f32_e32 v232, v232
	v_fma_f32 v235, v231, v235, v235
	v_min_f32_e32 v228, s42, v220
	v_rcp_f32_e32 v235, v235
	s_nop 0
	v_fma_f32 v231, -v233, v235, v235
	v_exp_f32_e32 v229, v221
	v_fma_f32 v201, v201, v232, v231
	v_exp_f32_e32 v231, v201
	v_exp_f32_e32 v228, v228
	v_add_f32_e32 v232, 1.0, v231
	v_fma_f32 v232, v234, v232, v232
	v_add_f32_e32 v227, 1.0, v227
	v_rcp_f32_e32 v232, v232
	v_mfma_f32_16x16x32_f16 v[146:149], v[114:117], v[158:161], v[146:149]
	v_fma_f32 v231, -v231, v232, v232
	v_fma_f32 v230, v228, s41, s41
	v_cvt_pk_f16_f32 v246, v226, v231
	v_mfma_f32_16x16x32_f16 v[146:149], v[118:121], v[162:165], v[146:149]
	v_exp_f32_e32 v231, v222
	v_rcp_f32_e32 v227, v227
	v_exp_f32_e32 v232, v223
	buffer_load_dwordx4 v[114:117], v189, s[16:19], s46 offen
	buffer_load_dwordx4 v[118:121], v208, s[16:19], s46 offen
	v_min_f32_e32 v233, s42, v224
	v_fma_f32 v230, v236, v230, v230
	v_exp_f32_e32 v234, v225
	s_waitcnt lgkmcnt(0)
	v_mfma_f32_16x16x32_f16 v[210:213], v[70:73], v[150:153], v[98:101]
	v_exp_f32_e32 v233, v233
	v_rcp_f32_e32 v230, v230
	v_add_f32_e32 v232, 1.0, v232
	v_mfma_f32_16x16x32_f16 v[214:217], v[74:77], v[150:153], v[102:105]
	v_fma_f32 v235, v233, s41, s41
	v_fma_f32 v236, -v228, v230, v230
	v_rcp_f32_e32 v232, v232
	v_fma_f32 v235, v231, v235, v235
	v_fma_f32 v198, v198, v227, v236
	v_rcp_f32_e32 v235, v235
	s_nop 0
	v_fma_f32 v231, -v233, v235, v235
	v_exp_f32_e32 v236, v198
	v_fma_f32 v199, v199, v232, v231
	v_exp_f32_e32 v231, v199
	v_add_f32_e32 v227, 1.0, v236
	v_add_f32_e32 v232, 1.0, v231
	v_fma_f32 v232, v234, v232, v232
	v_fma_f32 v227, v229, v227, v227
	v_rcp_f32_e32 v232, v232
	s_nop 0
	v_fma_f32 v231, -v231, v232, v232
	v_rcp_f32_e32 v227, v227
	s_nop 0
	v_fma_f32 v236, -v236, v227, v227
	v_cvt_pk_f16_f32 v247, v236, v231
	ds_write_b64 v206, v[246:247] offset:12288
	v_mfma_f32_16x16x32_f16 v[210:213], v[66:69], v[154:157], v[210:213]
	v_mfma_f32_16x16x32_f16 v[214:217], v[78:81], v[154:157], v[214:217]
	v_mov_b32_e32 v239, v246
	v_mov_b32_e32 v240, v247
	buffer_load_dwordx2 v[190:191], v209, s[20:23], s45 offen
	s_add_i32 s40, s40, 1
	s_add_i32 s44, s44, 0x1000
	s_waitcnt lgkmcnt(0)
	s_barrier
	ds_read_b128 v[158:161], v252 offset:4096
	ds_read_b128 v[162:165], v252 offset:5120
	ds_read_b128 v[166:169], v253 offset:6144
	ds_read_b128 v[170:173], v253 offset:7168
	v_mfma_f32_16x16x32_f16 v[218:221], v[82:85], v[150:153], v[106:109]
	v_mfma_f32_16x16x32_f16 v[222:225], v[90:93], v[150:153], v[110:113]
	v_mfma_f32_16x16x32_f16 v[218:221], v[86:89], v[154:157], v[218:221]
	v_mfma_f32_16x16x32_f16 v[222:225], v[94:97], v[154:157], v[222:225]
	s_waitcnt lgkmcnt(2)
	v_mfma_f32_16x16x32_f16 v[210:213], v[54:57], v[158:161], v[210:213]
	v_mfma_f32_16x16x32_f16 v[210:213], v[58:61], v[162:165], v[210:213]
	s_waitcnt lgkmcnt(0)
	v_mfma_f32_16x16x32_f16 v[210:213], v[62:65], v[166:169], v[210:213]
	v_mfma_f32_16x16x32_f16 v[210:213], v[50:53], v[170:173], v[210:213]
	s_waitcnt vmcnt(9)
	v_cvt_pk_f16_f32 v251, v196, v197
	ds_write_b32 v1, v251 offset:4096
	ds_read_b128 v[150:153], v186 offset:2048
	ds_read_b128 v[154:157], v186 offset:3072
	s_add_i32 s45, s45, 0x100000
	s_add_i32 s46, s46, 0x4000
	s_movk_i32 s47, 0x0
	s_add_i32 s43, s40, -12
	s_lshl_b32 s43, s43, 12
	s_cmp_lt_u32 s40, 14
	s_cselect_b32 s43, s47, s43
	v_exp_f32_e32 v226, v210
	v_exp_f32_e32 v227, v211
	v_mfma_f32_16x16x32_f16 v[214:217], v[34:37], v[158:161], v[214:217]
	v_min_f32_e32 v228, s42, v212
	v_exp_f32_e32 v229, v213
	v_mfma_f32_16x16x32_f16 v[214:217], v[38:41], v[162:165], v[214:217]
	v_exp_f32_e32 v228, v228
	v_add_f32_e32 v227, 1.0, v227
	v_mfma_f32_16x16x32_f16 v[214:217], v[42:45], v[166:169], v[214:217]
	v_fma_f32 v230, v228, s41, s41
	v_rcp_f32_e32 v227, v227
	v_mfma_f32_16x16x32_f16 v[214:217], v[46:49], v[170:173], v[214:217]
	v_fma_f32 v230, v226, v230, v230
	v_rcp_f32_e32 v230, v230
	v_mfma_f32_16x16x32_f16 v[218:221], v[18:21], v[158:161], v[218:221]
	v_fma_f32 v226, -v228, v230, v230
	v_fma_f32 v200, v200, v227, v226
	v_mfma_f32_16x16x32_f16 v[218:221], v[14:17], v[162:165], v[218:221]
	v_exp_f32_e32 v226, v200
	s_nop 0
	v_add_f32_e32 v227, 1.0, v226
	v_mfma_f32_16x16x32_f16 v[218:221], v[10:13], v[166:169], v[218:221]
	v_fma_f32 v227, v229, v227, v227
	v_rcp_f32_e32 v227, v227
	v_mfma_f32_16x16x32_f16 v[218:221], v[26:29], v[170:173], v[218:221]
	v_fma_f32 v226, -v226, v227, v227
	v_exp_f32_e32 v231, v214
	v_mfma_f32_16x16x32_f16 v[222:225], v[2:5], v[158:161], v[222:225]
	v_exp_f32_e32 v232, v215
	v_min_f32_e32 v233, s42, v216
	v_mfma_f32_16x16x32_f16 v[222:225], v[6:9], v[162:165], v[222:225]
	v_exp_f32_e32 v234, v217
	v_exp_f32_e32 v233, v233
	v_mfma_f32_16x16x32_f16 v[222:225], v[22:25], v[166:169], v[222:225]
	v_exp_f32_e32 v236, v218
	v_add_f32_e32 v232, 1.0, v232
	v_mfma_f32_16x16x32_f16 v[222:225], v[30:33], v[170:173], v[222:225]
	v_fma_f32 v235, v233, s41, s41
	v_exp_f32_e32 v227, v219
	v_rcp_f32_e32 v232, v232
	v_fma_f32 v235, v231, v235, v235
	v_min_f32_e32 v228, s42, v220
	v_rcp_f32_e32 v235, v235
	s_nop 0
	v_fma_f32 v231, -v233, v235, v235
	v_exp_f32_e32 v229, v221
	v_fma_f32 v201, v201, v232, v231
	v_exp_f32_e32 v231, v201
	v_exp_f32_e32 v228, v228
	v_add_f32_e32 v232, 1.0, v231
	v_fma_f32 v232, v234, v232, v232
	v_add_f32_e32 v227, 1.0, v227
	v_rcp_f32_e32 v232, v232
	v_mfma_f32_16x16x32_f16 v[146:149], v[138:141], v[158:161], v[146:149]
	v_fma_f32 v231, -v231, v232, v232
	v_fma_f32 v230, v228, s41, s41
	v_cvt_pk_f16_f32 v246, v226, v231
	v_mfma_f32_16x16x32_f16 v[146:149], v[142:145], v[162:165], v[146:149]
	v_exp_f32_e32 v231, v222
	v_rcp_f32_e32 v227, v227
	v_exp_f32_e32 v232, v223
	buffer_load_dwordx4 v[138:141], v189, s[16:19], s46 offen
	buffer_load_dwordx4 v[142:145], v208, s[16:19], s46 offen
	v_min_f32_e32 v233, s42, v224
	v_fma_f32 v230, v236, v230, v230
	v_exp_f32_e32 v234, v225
	s_waitcnt lgkmcnt(0)
	v_mfma_f32_16x16x32_f16 v[210:213], v[70:73], v[150:153], v[98:101]
	v_exp_f32_e32 v233, v233
	v_rcp_f32_e32 v230, v230
	v_add_f32_e32 v232, 1.0, v232
	v_mfma_f32_16x16x32_f16 v[214:217], v[74:77], v[150:153], v[102:105]
	v_fma_f32 v235, v233, s41, s41
	v_fma_f32 v236, -v228, v230, v230
	v_rcp_f32_e32 v232, v232
	v_fma_f32 v235, v231, v235, v235
	v_fma_f32 v198, v198, v227, v236
	v_rcp_f32_e32 v235, v235
	s_nop 0
	v_fma_f32 v231, -v233, v235, v235
	v_exp_f32_e32 v236, v198
	v_fma_f32 v199, v199, v232, v231
	v_exp_f32_e32 v231, v199
	v_add_f32_e32 v227, 1.0, v236
	v_add_f32_e32 v232, 1.0, v231
	v_fma_f32 v232, v234, v232, v232
	v_fma_f32 v227, v229, v227, v227
	v_rcp_f32_e32 v232, v232
	s_nop 0
	v_fma_f32 v231, -v231, v232, v232
	v_rcp_f32_e32 v227, v227
	s_nop 0
	v_fma_f32 v236, -v236, v227, v227
	v_cvt_pk_f16_f32 v247, v236, v231
	ds_write_b64 v206, v[246:247] offset:8192
	v_mfma_f32_16x16x32_f16 v[210:213], v[66:69], v[154:157], v[210:213]
	v_mfma_f32_16x16x32_f16 v[214:217], v[78:81], v[154:157], v[214:217]
	v_mov_b32_e32 v241, v246
	v_mov_b32_e32 v242, v247
	buffer_load_dwordx2 v[196:197], v209, s[20:23], s45 offen
	s_add_i32 s40, s40, 1
	s_add_i32 s44, s44, 0x1000
	s_waitcnt lgkmcnt(0)
	s_barrier
	ds_read_b128 v[158:161], v252 offset:0
	ds_read_b128 v[162:165], v252 offset:1024
	ds_read_b128 v[166:169], v253 offset:2048
	ds_read_b128 v[170:173], v253 offset:3072
	v_mfma_f32_16x16x32_f16 v[218:221], v[82:85], v[150:153], v[106:109]
	v_mfma_f32_16x16x32_f16 v[222:225], v[90:93], v[150:153], v[110:113]
	v_mfma_f32_16x16x32_f16 v[218:221], v[86:89], v[154:157], v[218:221]
	v_mfma_f32_16x16x32_f16 v[222:225], v[94:97], v[154:157], v[222:225]
	s_waitcnt lgkmcnt(2)
	v_mfma_f32_16x16x32_f16 v[210:213], v[54:57], v[158:161], v[210:213]
	v_mfma_f32_16x16x32_f16 v[210:213], v[58:61], v[162:165], v[210:213]
	s_waitcnt lgkmcnt(0)
	v_mfma_f32_16x16x32_f16 v[210:213], v[62:65], v[166:169], v[210:213]
	v_mfma_f32_16x16x32_f16 v[210:213], v[50:53], v[170:173], v[210:213]
	s_waitcnt vmcnt(9)
	v_cvt_pk_f16_f32 v251, v194, v195
	ds_write_b32 v1, v251 offset:6144
	ds_read_b128 v[150:153], v186 offset:4096
	ds_read_b128 v[154:157], v186 offset:5120
	s_add_i32 s45, s45, 0x100000
	s_add_i32 s46, s46, 0x4000
	s_movk_i32 s47, 0x1000
	s_add_i32 s43, s40, -12
	s_lshl_b32 s43, s43, 12
	s_cmp_lt_u32 s40, 14
	s_cselect_b32 s43, s47, s43
	v_exp_f32_e32 v226, v210
	v_exp_f32_e32 v227, v211
	v_mfma_f32_16x16x32_f16 v[214:217], v[34:37], v[158:161], v[214:217]
	v_min_f32_e32 v228, s42, v212
	v_exp_f32_e32 v229, v213
	v_mfma_f32_16x16x32_f16 v[214:217], v[38:41], v[162:165], v[214:217]
	v_exp_f32_e32 v228, v228
	v_add_f32_e32 v227, 1.0, v227
	v_mfma_f32_16x16x32_f16 v[214:217], v[42:45], v[166:169], v[214:217]
	v_fma_f32 v230, v228, s41, s41
	v_rcp_f32_e32 v227, v227
	v_mfma_f32_16x16x32_f16 v[214:217], v[46:49], v[170:173], v[214:217]
	v_fma_f32 v230, v226, v230, v230
	v_rcp_f32_e32 v230, v230
	v_mfma_f32_16x16x32_f16 v[218:221], v[18:21], v[158:161], v[218:221]
	v_fma_f32 v226, -v228, v230, v230
	v_fma_f32 v200, v200, v227, v226
	v_mfma_f32_16x16x32_f16 v[218:221], v[14:17], v[162:165], v[218:221]
	v_exp_f32_e32 v226, v200
	s_nop 0
	v_add_f32_e32 v227, 1.0, v226
	v_mfma_f32_16x16x32_f16 v[218:221], v[10:13], v[166:169], v[218:221]
	v_fma_f32 v227, v229, v227, v227
	v_rcp_f32_e32 v227, v227
	v_mfma_f32_16x16x32_f16 v[218:221], v[26:29], v[170:173], v[218:221]
	v_fma_f32 v226, -v226, v227, v227
	v_exp_f32_e32 v231, v214
	v_mfma_f32_16x16x32_f16 v[222:225], v[2:5], v[158:161], v[222:225]
	v_exp_f32_e32 v232, v215
	v_min_f32_e32 v233, s42, v216
	v_mfma_f32_16x16x32_f16 v[222:225], v[6:9], v[162:165], v[222:225]
	v_exp_f32_e32 v234, v217
	v_exp_f32_e32 v233, v233
	v_mfma_f32_16x16x32_f16 v[222:225], v[22:25], v[166:169], v[222:225]
	v_exp_f32_e32 v236, v218
	v_add_f32_e32 v232, 1.0, v232
	v_mfma_f32_16x16x32_f16 v[222:225], v[30:33], v[170:173], v[222:225]
	v_fma_f32 v235, v233, s41, s41
	v_exp_f32_e32 v227, v219
	v_rcp_f32_e32 v232, v232
	v_fma_f32 v235, v231, v235, v235
	v_min_f32_e32 v228, s42, v220
	v_rcp_f32_e32 v235, v235
	s_nop 0
	v_fma_f32 v231, -v233, v235, v235
	v_exp_f32_e32 v229, v221
	v_fma_f32 v201, v201, v232, v231
	v_exp_f32_e32 v231, v201
	v_exp_f32_e32 v228, v228
	v_add_f32_e32 v232, 1.0, v231
	v_fma_f32 v232, v234, v232, v232
	v_add_f32_e32 v227, 1.0, v227
	v_rcp_f32_e32 v232, v232
	v_mfma_f32_16x16x32_f16 v[146:149], v[130:133], v[158:161], v[146:149]
	v_fma_f32 v231, -v231, v232, v232
	v_fma_f32 v230, v228, s41, s41
	v_cvt_pk_f16_f32 v246, v226, v231
	v_mfma_f32_16x16x32_f16 v[146:149], v[134:137], v[162:165], v[146:149]
	v_exp_f32_e32 v231, v222
	v_rcp_f32_e32 v227, v227
	v_exp_f32_e32 v232, v223
	buffer_load_dwordx4 v[130:133], v189, s[16:19], s46 offen
	buffer_load_dwordx4 v[134:137], v208, s[16:19], s46 offen
	v_min_f32_e32 v233, s42, v224
	v_fma_f32 v230, v236, v230, v230
	v_exp_f32_e32 v234, v225
	s_waitcnt lgkmcnt(0)
	v_mfma_f32_16x16x32_f16 v[210:213], v[70:73], v[150:153], v[98:101]
	v_exp_f32_e32 v233, v233
	v_rcp_f32_e32 v230, v230
	v_add_f32_e32 v232, 1.0, v232
	v_mfma_f32_16x16x32_f16 v[214:217], v[74:77], v[150:153], v[102:105]
	v_fma_f32 v235, v233, s41, s41
	v_fma_f32 v236, -v228, v230, v230
	v_rcp_f32_e32 v232, v232
	v_fma_f32 v235, v231, v235, v235
	v_fma_f32 v198, v198, v227, v236
	v_rcp_f32_e32 v235, v235
	s_nop 0
	v_fma_f32 v231, -v233, v235, v235
	v_exp_f32_e32 v236, v198
	v_fma_f32 v199, v199, v232, v231
	v_exp_f32_e32 v231, v199
	v_add_f32_e32 v227, 1.0, v236
	v_add_f32_e32 v232, 1.0, v231
	v_fma_f32 v232, v234, v232, v232
	v_fma_f32 v227, v229, v227, v227
	v_rcp_f32_e32 v232, v232
	s_nop 0
	v_fma_f32 v231, -v231, v232, v232
	v_rcp_f32_e32 v227, v227
	s_nop 0
	v_fma_f32 v236, -v236, v227, v227
	v_cvt_pk_f16_f32 v247, v236, v231
	ds_write_b64 v206, v[246:247] offset:12288
	v_mfma_f32_16x16x32_f16 v[210:213], v[66:69], v[154:157], v[210:213]
	v_mfma_f32_16x16x32_f16 v[214:217], v[78:81], v[154:157], v[214:217]
	v_mov_b32_e32 v243, v246
	v_mov_b32_e32 v244, v247
	buffer_load_dwordx2 v[194:195], v209, s[20:23], s45 offen
	s_add_i32 s40, s40, 1
	s_add_i32 s44, s44, 0x1000
	s_waitcnt lgkmcnt(0)
	s_barrier
	ds_read_b128 v[158:161], v252 offset:4096
	ds_read_b128 v[162:165], v252 offset:5120
	ds_read_b128 v[166:169], v253 offset:6144
	ds_read_b128 v[170:173], v253 offset:7168
	v_mfma_f32_16x16x32_f16 v[218:221], v[82:85], v[150:153], v[106:109]
	v_mfma_f32_16x16x32_f16 v[222:225], v[90:93], v[150:153], v[110:113]
	v_mfma_f32_16x16x32_f16 v[218:221], v[86:89], v[154:157], v[218:221]
	v_mfma_f32_16x16x32_f16 v[222:225], v[94:97], v[154:157], v[222:225]
	s_waitcnt lgkmcnt(2)
	v_mfma_f32_16x16x32_f16 v[210:213], v[54:57], v[158:161], v[210:213]
	v_mfma_f32_16x16x32_f16 v[210:213], v[58:61], v[162:165], v[210:213]
	s_waitcnt lgkmcnt(0)
	v_mfma_f32_16x16x32_f16 v[210:213], v[62:65], v[166:169], v[210:213]
	v_mfma_f32_16x16x32_f16 v[210:213], v[50:53], v[170:173], v[210:213]
	s_waitcnt vmcnt(9)
	v_cvt_pk_f16_f32 v251, v192, v193
	ds_write_b32 v1, v251 offset:0
	ds_read_b128 v[150:153], v186 offset:6144
	ds_read_b128 v[154:157], v186 offset:7168
	s_add_i32 s45, s45, 0x100000
	s_add_i32 s46, s46, 0x4000
	s_movk_i32 s47, 0x0
	s_add_i32 s43, s40, -12
	s_lshl_b32 s43, s43, 12
	s_cmp_lt_u32 s40, 14
	s_cselect_b32 s43, s47, s43
	v_exp_f32_e32 v226, v210
	v_exp_f32_e32 v227, v211
	v_mfma_f32_16x16x32_f16 v[214:217], v[34:37], v[158:161], v[214:217]
	v_min_f32_e32 v228, s42, v212
	v_exp_f32_e32 v229, v213
	v_mfma_f32_16x16x32_f16 v[214:217], v[38:41], v[162:165], v[214:217]
	v_exp_f32_e32 v228, v228
	v_add_f32_e32 v227, 1.0, v227
	v_mfma_f32_16x16x32_f16 v[214:217], v[42:45], v[166:169], v[214:217]
	v_fma_f32 v230, v228, s41, s41
	v_rcp_f32_e32 v227, v227
	v_mfma_f32_16x16x32_f16 v[214:217], v[46:49], v[170:173], v[214:217]
	v_fma_f32 v230, v226, v230, v230
	v_rcp_f32_e32 v230, v230
	v_mfma_f32_16x16x32_f16 v[218:221], v[18:21], v[158:161], v[218:221]
	v_fma_f32 v226, -v228, v230, v230
	v_fma_f32 v200, v200, v227, v226
	v_mfma_f32_16x16x32_f16 v[218:221], v[14:17], v[162:165], v[218:221]
	v_exp_f32_e32 v226, v200
	s_nop 0
	v_add_f32_e32 v227, 1.0, v226
	v_mfma_f32_16x16x32_f16 v[218:221], v[10:13], v[166:169], v[218:221]
	v_fma_f32 v227, v229, v227, v227
	v_rcp_f32_e32 v227, v227
	v_mfma_f32_16x16x32_f16 v[218:221], v[26:29], v[170:173], v[218:221]
	v_fma_f32 v226, -v226, v227, v227
	v_exp_f32_e32 v231, v214
	v_mfma_f32_16x16x32_f16 v[222:225], v[2:5], v[158:161], v[222:225]
	v_exp_f32_e32 v232, v215
	v_min_f32_e32 v233, s42, v216
	v_mfma_f32_16x16x32_f16 v[222:225], v[6:9], v[162:165], v[222:225]
	v_exp_f32_e32 v234, v217
	v_exp_f32_e32 v233, v233
	v_mfma_f32_16x16x32_f16 v[222:225], v[22:25], v[166:169], v[222:225]
	v_exp_f32_e32 v236, v218
	v_add_f32_e32 v232, 1.0, v232
	v_mfma_f32_16x16x32_f16 v[222:225], v[30:33], v[170:173], v[222:225]
	v_fma_f32 v235, v233, s41, s41
	v_exp_f32_e32 v227, v219
	v_rcp_f32_e32 v232, v232
	v_fma_f32 v235, v231, v235, v235
	v_min_f32_e32 v228, s42, v220
	v_rcp_f32_e32 v235, v235
	s_nop 0
	v_fma_f32 v231, -v233, v235, v235
	v_exp_f32_e32 v229, v221
	v_fma_f32 v201, v201, v232, v231
	v_exp_f32_e32 v231, v201
	v_exp_f32_e32 v228, v228
	v_add_f32_e32 v232, 1.0, v231
	v_fma_f32 v232, v234, v232, v232
	v_add_f32_e32 v227, 1.0, v227
	v_rcp_f32_e32 v232, v232
	v_mfma_f32_16x16x32_f16 v[146:149], v[122:125], v[158:161], v[146:149]
	v_fma_f32 v231, -v231, v232, v232
	v_fma_f32 v230, v228, s41, s41
	v_cvt_pk_f16_f32 v246, v226, v231
	v_mfma_f32_16x16x32_f16 v[146:149], v[126:129], v[162:165], v[146:149]
	v_exp_f32_e32 v231, v222
	v_rcp_f32_e32 v227, v227
	v_exp_f32_e32 v232, v223
	buffer_load_dwordx4 v[122:125], v189, s[16:19], s46 offen
	buffer_load_dwordx4 v[126:129], v208, s[16:19], s46 offen
	v_min_f32_e32 v233, s42, v224
	v_fma_f32 v230, v236, v230, v230
	v_exp_f32_e32 v234, v225
	s_waitcnt lgkmcnt(0)
	v_mfma_f32_16x16x32_f16 v[210:213], v[70:73], v[150:153], v[98:101]
	v_exp_f32_e32 v233, v233
	v_rcp_f32_e32 v230, v230
	v_add_f32_e32 v232, 1.0, v232
	v_mfma_f32_16x16x32_f16 v[214:217], v[74:77], v[150:153], v[102:105]
	v_fma_f32 v235, v233, s41, s41
	v_fma_f32 v236, -v228, v230, v230
	v_rcp_f32_e32 v232, v232
	v_fma_f32 v235, v231, v235, v235
	v_fma_f32 v198, v198, v227, v236
	v_rcp_f32_e32 v235, v235
	s_nop 0
	v_fma_f32 v231, -v233, v235, v235
	v_exp_f32_e32 v236, v198
	v_fma_f32 v199, v199, v232, v231
	v_exp_f32_e32 v231, v199
	v_add_f32_e32 v227, 1.0, v236
	v_add_f32_e32 v232, 1.0, v231
	v_fma_f32 v232, v234, v232, v232
	v_fma_f32 v227, v229, v227, v227
	v_rcp_f32_e32 v232, v232
	s_nop 0
	v_fma_f32 v231, -v231, v232, v232
	v_rcp_f32_e32 v227, v227
	s_nop 0
	v_fma_f32 v236, -v236, v227, v227
	v_cvt_pk_f16_f32 v247, v236, v231
	ds_write_b64 v206, v[246:247] offset:8192
	v_mfma_f32_16x16x32_f16 v[210:213], v[66:69], v[154:157], v[210:213]
	v_mfma_f32_16x16x32_f16 v[214:217], v[78:81], v[154:157], v[214:217]
	v_mov_b32_e32 v245, v246
	v_mov_b32_e32 v187, v247
	buffer_load_dwordx2 v[192:193], v209, s[20:23], s45 offen
	s_add_i32 s40, s40, 1
	s_add_i32 s44, s44, 0x1000
	s_waitcnt lgkmcnt(0)
	s_barrier
	ds_read_b128 v[158:161], v252 offset:0
	ds_read_b128 v[162:165], v252 offset:1024
	ds_read_b128 v[166:169], v253 offset:2048
	ds_read_b128 v[170:173], v253 offset:3072
	v_mfma_f32_16x16x32_f16 v[218:221], v[82:85], v[150:153], v[106:109]
	v_mfma_f32_16x16x32_f16 v[222:225], v[90:93], v[150:153], v[110:113]
	v_mfma_f32_16x16x32_f16 v[218:221], v[86:89], v[154:157], v[218:221]
	v_mfma_f32_16x16x32_f16 v[222:225], v[94:97], v[154:157], v[222:225]
	s_waitcnt lgkmcnt(2)
	v_mfma_f32_16x16x32_f16 v[210:213], v[54:57], v[158:161], v[210:213]
	v_mfma_f32_16x16x32_f16 v[210:213], v[58:61], v[162:165], v[210:213]
	s_waitcnt lgkmcnt(0)
	v_mfma_f32_16x16x32_f16 v[210:213], v[62:65], v[166:169], v[210:213]
	v_mfma_f32_16x16x32_f16 v[210:213], v[50:53], v[170:173], v[210:213]
	s_waitcnt vmcnt(9)
	v_cvt_pk_f16_f32 v251, v190, v191
	ds_write_b32 v1, v251 offset:2048
	ds_read_b128 v[150:153], v186 offset:0
	ds_read_b128 v[154:157], v186 offset:1024
	s_add_i32 s45, s45, 0x100000
	s_add_i32 s46, s46, 0x4000
	s_movk_i32 s47, 0x1000
	s_add_i32 s43, s40, -12
	s_lshl_b32 s43, s43, 12
	s_cmp_lt_u32 s40, 14
	s_cselect_b32 s43, s47, s43
	v_exp_f32_e32 v226, v210
	v_exp_f32_e32 v227, v211
	v_mfma_f32_16x16x32_f16 v[214:217], v[34:37], v[158:161], v[214:217]
	v_min_f32_e32 v228, s42, v212
	v_exp_f32_e32 v229, v213
	v_mfma_f32_16x16x32_f16 v[214:217], v[38:41], v[162:165], v[214:217]
	v_exp_f32_e32 v228, v228
	v_add_f32_e32 v227, 1.0, v227
	v_mfma_f32_16x16x32_f16 v[214:217], v[42:45], v[166:169], v[214:217]
	v_fma_f32 v230, v228, s41, s41
	v_rcp_f32_e32 v227, v227
	v_mfma_f32_16x16x32_f16 v[214:217], v[46:49], v[170:173], v[214:217]
	v_fma_f32 v230, v226, v230, v230
	v_rcp_f32_e32 v230, v230
	v_mfma_f32_16x16x32_f16 v[218:221], v[18:21], v[158:161], v[218:221]
	v_fma_f32 v226, -v228, v230, v230
	v_fma_f32 v200, v200, v227, v226
	v_mfma_f32_16x16x32_f16 v[218:221], v[14:17], v[162:165], v[218:221]
	v_exp_f32_e32 v226, v200
	s_nop 0
	v_add_f32_e32 v227, 1.0, v226
	v_mfma_f32_16x16x32_f16 v[218:221], v[10:13], v[166:169], v[218:221]
	v_fma_f32 v227, v229, v227, v227
	v_rcp_f32_e32 v227, v227
	v_mfma_f32_16x16x32_f16 v[218:221], v[26:29], v[170:173], v[218:221]
	v_fma_f32 v226, -v226, v227, v227
	v_exp_f32_e32 v231, v214
	v_mfma_f32_16x16x32_f16 v[222:225], v[2:5], v[158:161], v[222:225]
	v_exp_f32_e32 v232, v215
	v_min_f32_e32 v233, s42, v216
	v_mfma_f32_16x16x32_f16 v[222:225], v[6:9], v[162:165], v[222:225]
	v_exp_f32_e32 v234, v217
	v_exp_f32_e32 v233, v233
	v_mfma_f32_16x16x32_f16 v[222:225], v[22:25], v[166:169], v[222:225]
	v_exp_f32_e32 v236, v218
	v_add_f32_e32 v232, 1.0, v232
	v_mfma_f32_16x16x32_f16 v[222:225], v[30:33], v[170:173], v[222:225]
	v_fma_f32 v235, v233, s41, s41
	v_exp_f32_e32 v227, v219
	v_rcp_f32_e32 v232, v232
	v_fma_f32 v235, v231, v235, v235
	v_min_f32_e32 v228, s42, v220
	v_rcp_f32_e32 v235, v235
	s_nop 0
	v_fma_f32 v231, -v233, v235, v235
	v_exp_f32_e32 v229, v221
	v_fma_f32 v201, v201, v232, v231
	v_exp_f32_e32 v231, v201
	v_exp_f32_e32 v228, v228
	v_add_f32_e32 v232, 1.0, v231
	v_fma_f32 v232, v234, v232, v232
	v_add_f32_e32 v227, 1.0, v227
	v_rcp_f32_e32 v232, v232
	v_mfma_f32_16x16x32_f16 v[146:149], v[114:117], v[158:161], v[146:149]
	v_fma_f32 v231, -v231, v232, v232
	v_fma_f32 v230, v228, s41, s41
	v_cvt_pk_f16_f32 v246, v226, v231
	v_mfma_f32_16x16x32_f16 v[146:149], v[118:121], v[162:165], v[146:149]
	v_exp_f32_e32 v231, v222
	v_rcp_f32_e32 v227, v227
	v_exp_f32_e32 v232, v223
	buffer_load_dwordx4 v[114:117], v189, s[16:19], s46 offen
	buffer_load_dwordx4 v[118:121], v208, s[16:19], s46 offen
	v_min_f32_e32 v233, s42, v224
	v_fma_f32 v230, v236, v230, v230
	v_exp_f32_e32 v234, v225
	s_waitcnt lgkmcnt(0)
	v_mfma_f32_16x16x32_f16 v[210:213], v[70:73], v[150:153], v[98:101]
	v_exp_f32_e32 v233, v233
	v_rcp_f32_e32 v230, v230
	v_add_f32_e32 v232, 1.0, v232
	v_mfma_f32_16x16x32_f16 v[214:217], v[74:77], v[150:153], v[102:105]
	v_fma_f32 v235, v233, s41, s41
	v_fma_f32 v236, -v228, v230, v230
	v_rcp_f32_e32 v232, v232
	v_fma_f32 v235, v231, v235, v235
	v_fma_f32 v198, v198, v227, v236
	v_rcp_f32_e32 v235, v235
	s_nop 0
	v_fma_f32 v231, -v233, v235, v235
	v_exp_f32_e32 v236, v198
	v_fma_f32 v199, v199, v232, v231
	v_exp_f32_e32 v231, v199
	v_add_f32_e32 v227, 1.0, v236
	v_add_f32_e32 v232, 1.0, v231
	v_fma_f32 v232, v234, v232, v232
	v_fma_f32 v227, v229, v227, v227
	v_rcp_f32_e32 v232, v232
	s_nop 0
	v_fma_f32 v231, -v231, v232, v232
	v_rcp_f32_e32 v227, v227
	s_nop 0
	v_fma_f32 v236, -v236, v227, v227
	v_cvt_pk_f16_f32 v247, v236, v231
	ds_write_b64 v206, v[246:247] offset:12288
	v_mfma_f32_16x16x32_f16 v[210:213], v[66:69], v[154:157], v[210:213]
	v_mfma_f32_16x16x32_f16 v[214:217], v[78:81], v[154:157], v[214:217]
	v_mov_b32_e32 v188, v246
	v_mov_b32_e32 v202, v247
	buffer_load_dwordx2 v[190:191], v209, s[20:23], s45 offen
	s_add_i32 s40, s40, 1
	s_add_i32 s44, s44, 0x1000
	s_waitcnt lgkmcnt(0)
	s_barrier
	ds_read_b128 v[158:161], v252 offset:4096
	ds_read_b128 v[162:165], v252 offset:5120
	ds_read_b128 v[166:169], v253 offset:6144
	ds_read_b128 v[170:173], v253 offset:7168
	v_mfma_f32_16x16x32_f16 v[218:221], v[82:85], v[150:153], v[106:109]
	v_mfma_f32_16x16x32_f16 v[222:225], v[90:93], v[150:153], v[110:113]
	v_mfma_f32_16x16x32_f16 v[218:221], v[86:89], v[154:157], v[218:221]
	v_mfma_f32_16x16x32_f16 v[222:225], v[94:97], v[154:157], v[222:225]
	s_waitcnt lgkmcnt(2)
	v_mfma_f32_16x16x32_f16 v[210:213], v[54:57], v[158:161], v[210:213]
	v_mfma_f32_16x16x32_f16 v[210:213], v[58:61], v[162:165], v[210:213]
	s_waitcnt lgkmcnt(0)
	v_mfma_f32_16x16x32_f16 v[210:213], v[62:65], v[166:169], v[210:213]
	v_mfma_f32_16x16x32_f16 v[210:213], v[50:53], v[170:173], v[210:213]
	s_waitcnt vmcnt(9)
	v_cvt_pk_f16_f32 v251, v196, v197
	ds_write_b32 v1, v251 offset:4096
	ds_read_b128 v[150:153], v186 offset:2048
	ds_read_b128 v[154:157], v186 offset:3072
	s_add_i32 s45, s45, 0x100000
	s_add_i32 s46, s46, 0x4000
	s_movk_i32 s47, 0x0
	s_add_i32 s43, s40, -12
	s_lshl_b32 s43, s43, 12
	s_cmp_lt_u32 s40, 14
	s_cselect_b32 s43, s47, s43
	v_exp_f32_e32 v226, v210
	v_exp_f32_e32 v227, v211
	v_mfma_f32_16x16x32_f16 v[214:217], v[34:37], v[158:161], v[214:217]
	v_min_f32_e32 v228, s42, v212
	v_exp_f32_e32 v229, v213
	v_mfma_f32_16x16x32_f16 v[214:217], v[38:41], v[162:165], v[214:217]
	v_exp_f32_e32 v228, v228
	v_add_f32_e32 v227, 1.0, v227
	v_mfma_f32_16x16x32_f16 v[214:217], v[42:45], v[166:169], v[214:217]
	v_fma_f32 v230, v228, s41, s41
	v_rcp_f32_e32 v227, v227
	v_mfma_f32_16x16x32_f16 v[214:217], v[46:49], v[170:173], v[214:217]
	v_fma_f32 v230, v226, v230, v230
	v_rcp_f32_e32 v230, v230
	v_mfma_f32_16x16x32_f16 v[218:221], v[18:21], v[158:161], v[218:221]
	v_fma_f32 v226, -v228, v230, v230
	v_fma_f32 v200, v200, v227, v226
	v_mfma_f32_16x16x32_f16 v[218:221], v[14:17], v[162:165], v[218:221]
	v_exp_f32_e32 v226, v200
	s_nop 0
	v_add_f32_e32 v227, 1.0, v226
	v_mfma_f32_16x16x32_f16 v[218:221], v[10:13], v[166:169], v[218:221]
	v_fma_f32 v227, v229, v227, v227
	v_rcp_f32_e32 v227, v227
	v_mfma_f32_16x16x32_f16 v[218:221], v[26:29], v[170:173], v[218:221]
	v_fma_f32 v226, -v226, v227, v227
	v_exp_f32_e32 v231, v214
	v_mfma_f32_16x16x32_f16 v[222:225], v[2:5], v[158:161], v[222:225]
	v_exp_f32_e32 v232, v215
	v_min_f32_e32 v233, s42, v216
	v_mfma_f32_16x16x32_f16 v[222:225], v[6:9], v[162:165], v[222:225]
	v_exp_f32_e32 v234, v217
	v_exp_f32_e32 v233, v233
	v_mfma_f32_16x16x32_f16 v[222:225], v[22:25], v[166:169], v[222:225]
	v_exp_f32_e32 v236, v218
	v_add_f32_e32 v232, 1.0, v232
	v_mfma_f32_16x16x32_f16 v[222:225], v[30:33], v[170:173], v[222:225]
	v_fma_f32 v235, v233, s41, s41
	v_exp_f32_e32 v227, v219
	v_rcp_f32_e32 v232, v232
	v_fma_f32 v235, v231, v235, v235
	v_min_f32_e32 v228, s42, v220
	v_rcp_f32_e32 v235, v235
	s_nop 0
	v_fma_f32 v231, -v233, v235, v235
	v_exp_f32_e32 v229, v221
	v_fma_f32 v201, v201, v232, v231
	v_exp_f32_e32 v231, v201
	v_exp_f32_e32 v228, v228
	v_add_f32_e32 v232, 1.0, v231
	v_fma_f32 v232, v234, v232, v232
	v_add_f32_e32 v227, 1.0, v227
	v_rcp_f32_e32 v232, v232
	v_mfma_f32_16x16x32_f16 v[146:149], v[138:141], v[158:161], v[146:149]
	v_fma_f32 v231, -v231, v232, v232
	v_fma_f32 v230, v228, s41, s41
	v_cvt_pk_f16_f32 v246, v226, v231
	v_mfma_f32_16x16x32_f16 v[146:149], v[142:145], v[162:165], v[146:149]
	v_exp_f32_e32 v231, v222
	v_rcp_f32_e32 v227, v227
	v_exp_f32_e32 v232, v223
	buffer_load_dwordx4 v[138:141], v189, s[16:19], s46 offen
	buffer_load_dwordx4 v[142:145], v208, s[16:19], s46 offen
	v_min_f32_e32 v233, s42, v224
	v_fma_f32 v230, v236, v230, v230
	v_exp_f32_e32 v234, v225
	s_waitcnt lgkmcnt(0)
	v_mfma_f32_16x16x32_f16 v[210:213], v[70:73], v[150:153], v[98:101]
	v_exp_f32_e32 v233, v233
	v_rcp_f32_e32 v230, v230
	v_add_f32_e32 v232, 1.0, v232
	v_mfma_f32_16x16x32_f16 v[214:217], v[74:77], v[150:153], v[102:105]
	v_fma_f32 v235, v233, s41, s41
	v_fma_f32 v236, -v228, v230, v230
	v_rcp_f32_e32 v232, v232
	v_fma_f32 v235, v231, v235, v235
	v_fma_f32 v198, v198, v227, v236
	v_rcp_f32_e32 v235, v235
	s_nop 0
	v_fma_f32 v231, -v233, v235, v235
	v_exp_f32_e32 v236, v198
	v_fma_f32 v199, v199, v232, v231
	v_exp_f32_e32 v231, v199
	v_add_f32_e32 v227, 1.0, v236
	v_add_f32_e32 v232, 1.0, v231
	v_fma_f32 v232, v234, v232, v232
	v_fma_f32 v227, v229, v227, v227
	v_rcp_f32_e32 v232, v232
	s_nop 0
	v_fma_f32 v231, -v231, v232, v232
	v_rcp_f32_e32 v227, v227
	s_nop 0
	v_fma_f32 v236, -v236, v227, v227
	v_cvt_pk_f16_f32 v247, v236, v231
	ds_write_b64 v206, v[246:247] offset:8192
	v_mfma_f32_16x16x32_f16 v[210:213], v[66:69], v[154:157], v[210:213]
	v_mfma_f32_16x16x32_f16 v[214:217], v[78:81], v[154:157], v[214:217]
	v_mov_b32_e32 v203, v246
	v_mov_b32_e32 v204, v247
	buffer_load_dwordx2 v[196:197], v209, s[20:23], s45 offen
	s_add_i32 s40, s40, 1
	s_add_i32 s44, s44, 0x1000
	s_waitcnt lgkmcnt(0)
	s_barrier
	ds_read_b128 v[158:161], v252 offset:0
	ds_read_b128 v[162:165], v252 offset:1024
	ds_read_b128 v[166:169], v253 offset:2048
	ds_read_b128 v[170:173], v253 offset:3072
	v_mfma_f32_16x16x32_f16 v[218:221], v[82:85], v[150:153], v[106:109]
	v_mfma_f32_16x16x32_f16 v[222:225], v[90:93], v[150:153], v[110:113]
	v_mfma_f32_16x16x32_f16 v[218:221], v[86:89], v[154:157], v[218:221]
	v_mfma_f32_16x16x32_f16 v[222:225], v[94:97], v[154:157], v[222:225]
	s_waitcnt lgkmcnt(2)
	v_mfma_f32_16x16x32_f16 v[210:213], v[54:57], v[158:161], v[210:213]
	v_mfma_f32_16x16x32_f16 v[210:213], v[58:61], v[162:165], v[210:213]
	s_waitcnt lgkmcnt(0)
	v_mfma_f32_16x16x32_f16 v[210:213], v[62:65], v[166:169], v[210:213]
	v_mfma_f32_16x16x32_f16 v[210:213], v[50:53], v[170:173], v[210:213]
	s_waitcnt vmcnt(9)
	v_cvt_pk_f16_f32 v251, v194, v195
	ds_write_b32 v1, v251 offset:6144
	ds_read_b128 v[150:153], v186 offset:4096
	ds_read_b128 v[154:157], v186 offset:5120
	s_add_i32 s45, s45, 0x100000
	s_add_i32 s46, s46, 0x4000
	s_movk_i32 s47, 0x1000
	s_add_i32 s43, s40, -12
	s_lshl_b32 s43, s43, 12
	s_cmp_lt_u32 s40, 14
	s_cselect_b32 s43, s47, s43
	v_exp_f32_e32 v226, v210
	v_exp_f32_e32 v227, v211
	v_mfma_f32_16x16x32_f16 v[214:217], v[34:37], v[158:161], v[214:217]
	v_min_f32_e32 v228, s42, v212
	v_exp_f32_e32 v229, v213
	v_mfma_f32_16x16x32_f16 v[214:217], v[38:41], v[162:165], v[214:217]
	v_exp_f32_e32 v228, v228
	v_add_f32_e32 v227, 1.0, v227
	v_mfma_f32_16x16x32_f16 v[214:217], v[42:45], v[166:169], v[214:217]
	v_fma_f32 v230, v228, s41, s41
	v_rcp_f32_e32 v227, v227
	v_mfma_f32_16x16x32_f16 v[214:217], v[46:49], v[170:173], v[214:217]
	v_fma_f32 v230, v226, v230, v230
	v_rcp_f32_e32 v230, v230
	v_mfma_f32_16x16x32_f16 v[218:221], v[18:21], v[158:161], v[218:221]
	v_fma_f32 v226, -v228, v230, v230
	v_fma_f32 v200, v200, v227, v226
	v_mfma_f32_16x16x32_f16 v[218:221], v[14:17], v[162:165], v[218:221]
	v_exp_f32_e32 v226, v200
	s_nop 0
	v_add_f32_e32 v227, 1.0, v226
	v_mfma_f32_16x16x32_f16 v[218:221], v[10:13], v[166:169], v[218:221]
	v_fma_f32 v227, v229, v227, v227
	v_rcp_f32_e32 v227, v227
	v_mfma_f32_16x16x32_f16 v[218:221], v[26:29], v[170:173], v[218:221]
	v_fma_f32 v226, -v226, v227, v227
	v_exp_f32_e32 v231, v214
	v_mfma_f32_16x16x32_f16 v[222:225], v[2:5], v[158:161], v[222:225]
	v_exp_f32_e32 v232, v215
	v_min_f32_e32 v233, s42, v216
	v_mfma_f32_16x16x32_f16 v[222:225], v[6:9], v[162:165], v[222:225]
	v_exp_f32_e32 v234, v217
	v_exp_f32_e32 v233, v233
	v_mfma_f32_16x16x32_f16 v[222:225], v[22:25], v[166:169], v[222:225]
	v_exp_f32_e32 v236, v218
	v_add_f32_e32 v232, 1.0, v232
	v_mfma_f32_16x16x32_f16 v[222:225], v[30:33], v[170:173], v[222:225]
	v_fma_f32 v235, v233, s41, s41
	v_exp_f32_e32 v227, v219
	v_rcp_f32_e32 v232, v232
	v_fma_f32 v235, v231, v235, v235
	v_min_f32_e32 v228, s42, v220
	v_rcp_f32_e32 v235, v235
	s_nop 0
	v_fma_f32 v231, -v233, v235, v235
	v_exp_f32_e32 v229, v221
	v_fma_f32 v201, v201, v232, v231
	v_exp_f32_e32 v231, v201
	v_exp_f32_e32 v228, v228
	v_add_f32_e32 v232, 1.0, v231
	v_fma_f32 v232, v234, v232, v232
	v_add_f32_e32 v227, 1.0, v227
	v_rcp_f32_e32 v232, v232
	v_mfma_f32_16x16x32_f16 v[146:149], v[130:133], v[158:161], v[146:149]
	v_fma_f32 v231, -v231, v232, v232
	v_fma_f32 v230, v228, s41, s41
	v_cvt_pk_f16_f32 v246, v226, v231
	v_mfma_f32_16x16x32_f16 v[146:149], v[134:137], v[162:165], v[146:149]
	v_exp_f32_e32 v231, v222
	v_rcp_f32_e32 v227, v227
	v_exp_f32_e32 v232, v223
	buffer_load_dwordx4 v[130:133], v189, s[16:19], s46 offen
	buffer_load_dwordx4 v[134:137], v208, s[16:19], s46 offen
	v_min_f32_e32 v233, s42, v224
	v_fma_f32 v230, v236, v230, v230
	v_exp_f32_e32 v234, v225
	s_waitcnt lgkmcnt(0)
	v_mfma_f32_16x16x32_f16 v[210:213], v[70:73], v[150:153], v[98:101]
	v_exp_f32_e32 v233, v233
	v_rcp_f32_e32 v230, v230
	v_add_f32_e32 v232, 1.0, v232
	v_mfma_f32_16x16x32_f16 v[214:217], v[74:77], v[150:153], v[102:105]
	v_fma_f32 v235, v233, s41, s41
	v_fma_f32 v236, -v228, v230, v230
	v_rcp_f32_e32 v232, v232
	v_fma_f32 v235, v231, v235, v235
	v_fma_f32 v198, v198, v227, v236
	v_rcp_f32_e32 v235, v235
	s_nop 0
	v_fma_f32 v231, -v233, v235, v235
	v_exp_f32_e32 v236, v198
	v_fma_f32 v199, v199, v232, v231
	v_exp_f32_e32 v231, v199
	v_add_f32_e32 v227, 1.0, v236
	v_add_f32_e32 v232, 1.0, v231
	v_fma_f32 v232, v234, v232, v232
	v_fma_f32 v227, v229, v227, v227
	v_rcp_f32_e32 v232, v232
	s_nop 0
	v_fma_f32 v231, -v231, v232, v232
	v_rcp_f32_e32 v227, v227
	s_nop 0
	v_fma_f32 v236, -v236, v227, v227
	v_cvt_pk_f16_f32 v247, v236, v231
	ds_write_b64 v206, v[246:247] offset:12288
	v_mfma_f32_16x16x32_f16 v[210:213], v[66:69], v[154:157], v[210:213]
	v_mfma_f32_16x16x32_f16 v[214:217], v[78:81], v[154:157], v[214:217]
	v_mov_b32_e32 v205, v246
	v_mov_b32_e32 v207, v247
	buffer_load_dwordx2 v[194:195], v209, s[20:23], s45 offen
	s_add_i32 s40, s40, 1
	s_add_i32 s44, s44, 0x1000
	s_waitcnt lgkmcnt(0)
	s_barrier
	v_add_u32_e32 v250, 0x1000, v206
	v_add_u32_e32 v248, 0x1000, v252
	v_add_u32_e32 v249, 0x1000, v253
	s_mov_b32 s45, 0xc00000
	s_mov_b32 s46, 0x30000
